# strategy 4 setprio A/B: v32 with the mid-section s_setprio 0/1 flip pair removed in all four GEMM K-loops
# speedup vs baseline: 1.0001x; 1.0001x over previous
; #define PG8_STAGE(bufoff, gbase, voff) do { _Pragma("unroll") for (int _i = 0; _i < 2; ++_i) \
;         __builtin_amdgcn_global_load_lds((const unsigned*)((const char*)(gbase) + (voff)[_i]), (LAS unsigned*)(lds + (bufoff) + ldsw + _i * 8192), 16, 0, 0); } while (0)
; #define PG8_LDA(dst, b, h) do { _Pragma("unroll") for (int m = 0; m < 4; ++m) _Pragma("unroll") for (int k = 0; k < 2; ++k) dst[m][k] = *(const LAS bf16x8*)(lds + PG8_SA(b, h) + aoff + m * 2048 + k * 1024); } while (0)
; #define PG8_LDB(dst, b, h) do { _Pragma("unroll") for (int n = 0; n < 2; ++n) _Pragma("unroll") for (int k = 0; k < 2; ++k) dst[n][k] = *(const LAS bf16x8*)(lds + PG8_SB(b, h) + boff + n * 2048 + k * 1024); } while (0)
; #define PG8_MMA(ai, bj, At, Bt) do { __builtin_amdgcn_s_setprio(1); _Pragma("unroll") for (int m = 0; m < 4; ++m) _Pragma("unroll") for (int n = 0; n < 2; ++n) _Pragma("unroll") for (int k = 0; k < 2; ++k) \
;         acc[ai][bj][m][n] = __builtin_amdgcn_mfma_f32_16x16x32_bf16(Bt[n][k], At[m][k], acc[ai][bj][m][n], 0, 0, 0); __builtin_amdgcn_s_setprio(0); } while (0)
; #define PG8_WAIT_V(n) asm volatile("s_waitcnt vmcnt(" #n ")" ::: "memory")
; #define PG8_WAIT_L(n) asm volatile("s_waitcnt lgkmcnt(" #n ")" ::: "memory")
; #define PG8_BAR __builtin_amdgcn_s_barrier()
; #define PG8_SCHED __builtin_amdgcn_sched_barrier(0)
; #define PG8_STAGE(bufoff, gbase, voff) do { _Pragma("unroll") for (int _i = 0; _i < 2; ++_i) \
;         __builtin_amdgcn_global_load_lds((const unsigned*)((const char*)(gbase) + (voff)[_i]), (LAS unsigned*)(lds + (bufoff) + ldsw + _i * 8192), 16, 0, 0); } while (0)
; #define PG8_LDA(dst, b, h) do { _Pragma("unroll") for (int m = 0; m < 4; ++m) _Pragma("unroll") for (int k = 0; k < 2; ++k) dst[m][k] = *(const LAS bf16x8*)(lds + PG8_SA(b, h) + aoff + m * 2048 + k * 1024); } while (0)
;     ...
;             PG8_LDB(B0, 0, 0); PG8_LDB(B1, 0, 1); PG8_SCHED; PG8_LDA(At, 0, 0); PG8_STAGE(PG8_SA(1, 1), a1 + hstepA, voffA);
;             PG8_WAIT_V(8); PG8_WAIT_L(0); PG8_BAR; PG8_MMA(0, 0, At, B0); PG8_MMA(0, 1, At, B1); PG8_BAR; PG8_SCHED;
;             PG8_LDA(At, 0, 1); PG8_STAGE(PG8_SB(0, 0), b2, voffB); PG8_STAGE(PG8_SB(0, 1), b2 + hstep, voffB); PG8_STAGE(PG8_SA(0, 0), a2, voffA);
;             PG8_WAIT_V(8); PG8_WAIT_L(0); PG8_BAR; if (hi_on) { PG8_MMA(1, 0, At, B0); PG8_MMA(1, 1, At, B1); } PG8_BAR; PG8_SCHED;
.LBB0_213:
	s_add_u32 s22, s6, 0xfffc0080
	s_addc_u32 s23, s7, -1
	s_add_i32 s27, 0, 0x10000
	s_cmp_eq_u32 s26, 12
	s_cselect_b32 s25, s19, s23
	s_cselect_b32 s24, s18, s22
	v_add_u32_e32 v52, s27, v1
	s_cselect_b32 s23, s21, s17
	s_cselect_b32 s22, s20, s15
	s_add_i32 s42, 0, 0x14000
	ds_read_b128 v[62:65], v52
	ds_read_b128 v[66:69], v52 offset:1024
	ds_read_b128 v[156:159], v52 offset:2048
	ds_read_b128 v[160:163], v52 offset:3072
	v_add_u32_e32 v52, s42, v1
	ds_read_b128 v[168:171], v52
	ds_read_b128 v[172:175], v52 offset:1024
	ds_read_b128 v[176:179], v52 offset:2048
	ds_read_b128 v[180:183], v52 offset:3072
	v_lshl_add_u64 v[52:53], s[6:7], 0, v[152:153]
	s_add_i32 m0, s30, 0xc000
	ds_read_b128 v[184:187], v166
	ds_read_b128 v[188:191], v166 offset:1024
	ds_read_b128 v[192:195], v166 offset:2048
	ds_read_b128 v[204:207], v166 offset:3072
	ds_read_b128 v[208:211], v166 offset:4096
	ds_read_b128 v[212:215], v166 offset:5120
	ds_read_b128 v[216:219], v166 offset:6144
	ds_read_b128 v[220:223], v166 offset:7168
	global_load_lds_dwordx4 v[52:53], off
	v_lshl_add_u64 v[52:53], s[6:7], 0, v[154:155]
	s_add_i32 m0, s30, 0xe000
	s_nop 0
	global_load_lds_dwordx4 v[52:53], off
	s_waitcnt vmcnt(8)
	s_waitcnt lgkmcnt(0)
	s_barrier
	s_setprio 1
	s_waitcnt lgkmcnt(0)
	v_mfma_f32_16x16x32_bf16 v[138:141], v[62:65], v[184:187], v[138:141]
	v_mfma_f32_16x16x32_bf16 v[134:137], v[156:159], v[184:187], v[134:137]
	v_mfma_f32_16x16x32_bf16 v[122:125], v[62:65], v[192:195], v[122:125]
	v_mfma_f32_16x16x32_bf16 v[118:121], v[156:159], v[192:195], v[118:121]
	v_mfma_f32_16x16x32_bf16 v[106:109], v[62:65], v[208:211], v[106:109]
	v_mfma_f32_16x16x32_bf16 v[102:105], v[156:159], v[208:211], v[102:105]
	v_mfma_f32_16x16x32_bf16 v[90:93], v[62:65], v[216:219], v[90:93]
	v_mfma_f32_16x16x32_bf16 v[86:89], v[156:159], v[216:219], v[86:89]
	v_mfma_f32_16x16x32_bf16 v[138:141], v[66:69], v[188:191], v[138:141]
	v_mfma_f32_16x16x32_bf16 v[134:137], v[160:163], v[188:191], v[134:137]
	v_mfma_f32_16x16x32_bf16 v[122:125], v[66:69], v[204:207], v[122:125]
	v_mfma_f32_16x16x32_bf16 v[118:121], v[160:163], v[204:207], v[118:121]
	v_mfma_f32_16x16x32_bf16 v[106:109], v[66:69], v[212:215], v[106:109]
	v_mfma_f32_16x16x32_bf16 v[102:105], v[160:163], v[212:215], v[102:105]
	v_mfma_f32_16x16x32_bf16 v[90:93], v[66:69], v[220:223], v[90:93]
	v_mfma_f32_16x16x32_bf16 v[86:89], v[160:163], v[220:223], v[86:89]
	v_mfma_f32_16x16x32_bf16 v[130:133], v[168:171], v[184:187], v[130:133]
	v_mfma_f32_16x16x32_bf16 v[126:129], v[176:179], v[184:187], v[126:129]
	v_mfma_f32_16x16x32_bf16 v[114:117], v[168:171], v[192:195], v[114:117]
	v_mfma_f32_16x16x32_bf16 v[110:113], v[176:179], v[192:195], v[110:113]
	v_mfma_f32_16x16x32_bf16 v[98:101], v[168:171], v[208:211], v[98:101]
	v_mfma_f32_16x16x32_bf16 v[94:97], v[176:179], v[208:211], v[94:97]
	v_mfma_f32_16x16x32_bf16 v[82:85], v[168:171], v[216:219], v[82:85]
	v_mfma_f32_16x16x32_bf16 v[78:81], v[176:179], v[216:219], v[78:81]
	v_mfma_f32_16x16x32_bf16 v[130:133], v[172:175], v[188:191], v[130:133]
	v_mfma_f32_16x16x32_bf16 v[126:129], v[180:183], v[188:191], v[126:129]
	v_mfma_f32_16x16x32_bf16 v[114:117], v[172:175], v[204:207], v[114:117]
	v_mfma_f32_16x16x32_bf16 v[110:113], v[180:183], v[204:207], v[110:113]
	v_mfma_f32_16x16x32_bf16 v[98:101], v[172:175], v[212:215], v[98:101]
	v_mfma_f32_16x16x32_bf16 v[94:97], v[180:183], v[212:215], v[94:97]
	v_mfma_f32_16x16x32_bf16 v[82:85], v[172:175], v[220:223], v[82:85]
	v_mfma_f32_16x16x32_bf16 v[78:81], v[180:183], v[220:223], v[78:81]
	s_setprio 0
	s_barrier
	s_add_i32 s27, s27, s29
	v_lshl_add_u64 v[196:197], s[22:23], 0, v[144:145]
	s_mov_b32 m0, s27
	ds_read_b128 v[184:187], v166 offset:16384
	ds_read_b128 v[188:191], v166 offset:17408
	ds_read_b128 v[192:195], v166 offset:18432
	ds_read_b128 v[204:207], v166 offset:19456
	ds_read_b128 v[208:211], v166 offset:20480
	ds_read_b128 v[212:215], v166 offset:21504
	ds_read_b128 v[216:219], v166 offset:22528
	ds_read_b128 v[220:223], v166 offset:23552
	global_load_lds_dwordx4 v[196:197], off
	s_add_i32 m0, s27, 0x2000
	s_add_u32 s36, s22, 0x40000
	v_lshl_add_u64 v[224:225], s[22:23], 0, v[148:149]
	s_addc_u32 s37, s23, 0
	s_add_i32 s27, s42, s29
	global_load_lds_dwordx4 v[224:225], off
	v_lshl_add_u64 v[52:53], s[36:37], 0, v[144:145]
	s_mov_b32 m0, s27
	v_lshl_add_u64 v[226:227], s[24:25], 0, v[142:143]
	global_load_lds_dwordx4 v[52:53], off
	v_lshl_add_u64 v[52:53], s[36:37], 0, v[148:149]
	s_add_i32 m0, s27, 0x2000
	v_lshl_add_u64 v[228:229], s[24:25], 0, v[146:147]
	global_load_lds_dwordx4 v[52:53], off
	s_mov_b32 m0, s30
	s_nop 0
	global_load_lds_dwordx4 v[226:227], off
	s_mov_b32 m0, s31
	s_nop 0
	global_load_lds_dwordx4 v[228:229], off
	s_waitcnt vmcnt(8)
	s_waitcnt lgkmcnt(0)
	s_barrier
; #define PG8_STAGE(bufoff, gbase, voff) do { _Pragma("unroll") for (int _i = 0; _i < 2; ++_i) \
;         __builtin_amdgcn_global_load_lds((const unsigned*)((const char*)(gbase) + (voff)[_i]), (LAS unsigned*)(lds + (bufoff) + ldsw + _i * 8192), 16, 0, 0); } while (0)
; #define PG8_LDA(dst, b, h) do { _Pragma("unroll") for (int m = 0; m < 4; ++m) _Pragma("unroll") for (int k = 0; k < 2; ++k) dst[m][k] = *(const LAS bf16x8*)(lds + PG8_SA(b, h) + aoff + m * 2048 + k * 1024); } while (0)
; #define PG8_LDB(dst, b, h) do { _Pragma("unroll") for (int n = 0; n < 2; ++n) _Pragma("unroll") for (int k = 0; k < 2; ++k) dst[n][k] = *(const LAS bf16x8*)(lds + PG8_SB(b, h) + boff + n * 2048 + k * 1024); } while (0)
; #define PG8_MMA(ai, bj, At, Bt) do { __builtin_amdgcn_s_setprio(1); _Pragma("unroll") for (int m = 0; m < 4; ++m) _Pragma("unroll") for (int n = 0; n < 2; ++n) _Pragma("unroll") for (int k = 0; k < 2; ++k) \
;         acc[ai][bj][m][n] = __builtin_amdgcn_mfma_f32_16x16x32_bf16(Bt[n][k], At[m][k], acc[ai][bj][m][n], 0, 0, 0); __builtin_amdgcn_s_setprio(0); } while (0)
; #define PG8_WAIT_V(n) asm volatile("s_waitcnt vmcnt(" #n ")" ::: "memory")
; #define PG8_WAIT_L(n) asm volatile("s_waitcnt lgkmcnt(" #n ")" ::: "memory")
; #define PG8_BAR __builtin_amdgcn_s_barrier()
; #define PG8_SCHED __builtin_amdgcn_sched_barrier(0)
; #define PG8_STAGE(bufoff, gbase, voff) do { _Pragma("unroll") for (int _i = 0; _i < 2; ++_i) \
;         __builtin_amdgcn_global_load_lds((const unsigned*)((const char*)(gbase) + (voff)[_i]), (LAS unsigned*)(lds + (bufoff) + ldsw + _i * 8192), 16, 0, 0); } while (0)
; #define PG8_LDA(dst, b, h) do { _Pragma("unroll") for (int m = 0; m < 4; ++m) _Pragma("unroll") for (int k = 0; k < 2; ++k) dst[m][k] = *(const LAS bf16x8*)(lds + PG8_SA(b, h) + aoff + m * 2048 + k * 1024); } while (0)
;     ...
;             PG8_LDA(At, 0, 1); PG8_STAGE(PG8_SB(0, 0), b2, voffB); PG8_STAGE(PG8_SB(0, 1), b2 + hstep, voffB); PG8_STAGE(PG8_SA(0, 0), a2, voffA);
;             PG8_WAIT_V(8); PG8_WAIT_L(0); PG8_BAR; if (hi_on) { PG8_MMA(1, 0, At, B0); PG8_MMA(1, 1, At, B1); } PG8_BAR; PG8_SCHED;
;             PG8_LDB(B0, 1, 0); PG8_LDB(B1, 1, 1); PG8_SCHED; PG8_LDA(At, 1, 0); PG8_STAGE(PG8_SA(0, 1), a2 + hstepA, voffA);
;             PG8_WAIT_V(8); PG8_WAIT_L(0); PG8_BAR; PG8_MMA(0, 0, At, B0); PG8_MMA(0, 1, At, B1); PG8_BAR; PG8_SCHED;
	s_setprio 1
	s_waitcnt lgkmcnt(0)
	v_mfma_f32_16x16x32_bf16 v[74:77], v[62:65], v[184:187], v[74:77]
	v_mfma_f32_16x16x32_bf16 v[70:73], v[156:159], v[184:187], v[70:73]
	v_mfma_f32_16x16x32_bf16 v[48:51], v[62:65], v[192:195], v[48:51]
	v_mfma_f32_16x16x32_bf16 v[44:47], v[156:159], v[192:195], v[44:47]
	v_mfma_f32_16x16x32_bf16 v[30:33], v[62:65], v[208:211], v[30:33]
	v_mfma_f32_16x16x32_bf16 v[26:29], v[156:159], v[208:211], v[26:29]
	v_mfma_f32_16x16x32_bf16 v[14:17], v[62:65], v[216:219], v[14:17]
	v_mfma_f32_16x16x32_bf16 v[10:13], v[156:159], v[216:219], v[10:13]
	v_mfma_f32_16x16x32_bf16 v[74:77], v[66:69], v[188:191], v[74:77]
	v_mfma_f32_16x16x32_bf16 v[70:73], v[160:163], v[188:191], v[70:73]
	v_mfma_f32_16x16x32_bf16 v[48:51], v[66:69], v[204:207], v[48:51]
	v_mfma_f32_16x16x32_bf16 v[44:47], v[160:163], v[204:207], v[44:47]
	v_mfma_f32_16x16x32_bf16 v[30:33], v[66:69], v[212:215], v[30:33]
	v_mfma_f32_16x16x32_bf16 v[26:29], v[160:163], v[212:215], v[26:29]
	v_mfma_f32_16x16x32_bf16 v[14:17], v[66:69], v[220:223], v[14:17]
	v_mfma_f32_16x16x32_bf16 v[10:13], v[160:163], v[220:223], v[10:13]
	v_mfma_f32_16x16x32_bf16 v[58:61], v[168:171], v[184:187], v[58:61]
	v_mfma_f32_16x16x32_bf16 v[52:55], v[176:179], v[184:187], v[54:57]
	v_mfma_f32_16x16x32_bf16 v[40:43], v[168:171], v[192:195], v[40:43]
	v_mfma_f32_16x16x32_bf16 v[36:39], v[176:179], v[192:195], v[36:39]
	v_mfma_f32_16x16x32_bf16 v[22:25], v[168:171], v[208:211], v[22:25]
	v_mfma_f32_16x16x32_bf16 v[18:21], v[176:179], v[208:211], v[18:21]
	v_mfma_f32_16x16x32_bf16 v[6:9], v[168:171], v[216:219], v[6:9]
	v_mfma_f32_16x16x32_bf16 v[2:5], v[176:179], v[216:219], v[2:5]
	v_mfma_f32_16x16x32_bf16 v[58:61], v[172:175], v[188:191], v[58:61]
	v_mfma_f32_16x16x32_bf16 v[52:55], v[180:183], v[188:191], v[52:55]
	v_mfma_f32_16x16x32_bf16 v[40:43], v[172:175], v[204:207], v[40:43]
	v_mfma_f32_16x16x32_bf16 v[36:39], v[180:183], v[204:207], v[36:39]
	v_mfma_f32_16x16x32_bf16 v[22:25], v[172:175], v[212:215], v[22:25]
	v_mfma_f32_16x16x32_bf16 v[18:21], v[180:183], v[212:215], v[18:21]
	v_mfma_f32_16x16x32_bf16 v[6:9], v[172:175], v[220:223], v[6:9]
	v_mfma_f32_16x16x32_bf16 v[2:5], v[180:183], v[220:223], v[2:5]
	s_setprio 0
	s_barrier
	s_add_i32 s27, 0, 0x18000
	v_add_u32_e32 v56, s27, v1
	s_add_i32 s36, 0, 0x1c000
	ds_read_b128 v[62:65], v56
	ds_read_b128 v[66:69], v56 offset:1024
	ds_read_b128 v[156:159], v56 offset:2048
	ds_read_b128 v[160:163], v56 offset:3072
	v_add_u32_e32 v56, s36, v1
	ds_read_b128 v[168:171], v56
	ds_read_b128 v[172:175], v56 offset:1024
	ds_read_b128 v[176:179], v56 offset:2048
	ds_read_b128 v[180:183], v56 offset:3072
	s_add_u32 s24, s24, 0x40000
	s_addc_u32 s25, s25, 0
	s_mov_b32 m0, s34
	v_lshl_add_u64 v[56:57], s[24:25], 0, v[142:143]
	ds_read_b128 v[184:187], v166 offset:32768
	ds_read_b128 v[188:191], v166 offset:33792
	ds_read_b128 v[192:195], v166 offset:34816
	ds_read_b128 v[204:207], v166 offset:35840
	ds_read_b128 v[208:211], v166 offset:36864
	ds_read_b128 v[212:215], v166 offset:37888
	ds_read_b128 v[216:219], v166 offset:38912
	ds_read_b128 v[220:223], v166 offset:39936
	global_load_lds_dwordx4 v[56:57], off
	v_lshl_add_u64 v[56:57], s[24:25], 0, v[146:147]
	s_mov_b32 m0, s35
	s_nop 0
	global_load_lds_dwordx4 v[56:57], off
	s_waitcnt vmcnt(8)
	s_waitcnt lgkmcnt(0)
	s_barrier
	s_setprio 1
	s_waitcnt lgkmcnt(0)
	v_mfma_f32_16x16x32_bf16 v[138:141], v[62:65], v[184:187], v[138:141]
	v_mfma_f32_16x16x32_bf16 v[134:137], v[156:159], v[184:187], v[134:137]
	v_mfma_f32_16x16x32_bf16 v[122:125], v[62:65], v[192:195], v[122:125]
	v_mfma_f32_16x16x32_bf16 v[118:121], v[156:159], v[192:195], v[118:121]
	v_mfma_f32_16x16x32_bf16 v[106:109], v[62:65], v[208:211], v[106:109]
	v_mfma_f32_16x16x32_bf16 v[102:105], v[156:159], v[208:211], v[102:105]
	v_mfma_f32_16x16x32_bf16 v[90:93], v[62:65], v[216:219], v[90:93]
	v_mfma_f32_16x16x32_bf16 v[86:89], v[156:159], v[216:219], v[86:89]
	v_mfma_f32_16x16x32_bf16 v[138:141], v[66:69], v[188:191], v[138:141]
	v_mfma_f32_16x16x32_bf16 v[134:137], v[160:163], v[188:191], v[134:137]
	v_mfma_f32_16x16x32_bf16 v[122:125], v[66:69], v[204:207], v[122:125]
	v_mfma_f32_16x16x32_bf16 v[118:121], v[160:163], v[204:207], v[118:121]
	v_mfma_f32_16x16x32_bf16 v[106:109], v[66:69], v[212:215], v[106:109]
	v_mfma_f32_16x16x32_bf16 v[102:105], v[160:163], v[212:215], v[102:105]
	v_mfma_f32_16x16x32_bf16 v[90:93], v[66:69], v[220:223], v[90:93]
	v_mfma_f32_16x16x32_bf16 v[86:89], v[160:163], v[220:223], v[86:89]
	v_mfma_f32_16x16x32_bf16 v[130:133], v[168:171], v[184:187], v[130:133]
	v_mfma_f32_16x16x32_bf16 v[126:129], v[176:179], v[184:187], v[126:129]
	v_mfma_f32_16x16x32_bf16 v[114:117], v[168:171], v[192:195], v[114:117]
	v_mfma_f32_16x16x32_bf16 v[110:113], v[176:179], v[192:195], v[110:113]
	v_mfma_f32_16x16x32_bf16 v[98:101], v[168:171], v[208:211], v[98:101]
	v_mfma_f32_16x16x32_bf16 v[94:97], v[176:179], v[208:211], v[94:97]
	v_mfma_f32_16x16x32_bf16 v[82:85], v[168:171], v[216:219], v[82:85]
	v_mfma_f32_16x16x32_bf16 v[78:81], v[176:179], v[216:219], v[78:81]
	v_mfma_f32_16x16x32_bf16 v[130:133], v[172:175], v[188:191], v[130:133]
	v_mfma_f32_16x16x32_bf16 v[126:129], v[180:183], v[188:191], v[126:129]
	v_mfma_f32_16x16x32_bf16 v[114:117], v[172:175], v[204:207], v[114:117]
	v_mfma_f32_16x16x32_bf16 v[110:113], v[180:183], v[204:207], v[110:113]
	v_mfma_f32_16x16x32_bf16 v[98:101], v[172:175], v[212:215], v[98:101]
	v_mfma_f32_16x16x32_bf16 v[94:97], v[180:183], v[212:215], v[94:97]
	v_mfma_f32_16x16x32_bf16 v[82:85], v[172:175], v[220:223], v[82:85]
	v_mfma_f32_16x16x32_bf16 v[78:81], v[180:183], v[220:223], v[78:81]
	s_setprio 0
	s_barrier
; #define PG8_STAGE(bufoff, gbase, voff) do { _Pragma("unroll") for (int _i = 0; _i < 2; ++_i) \
;         __builtin_amdgcn_global_load_lds((const unsigned*)((const char*)(gbase) + (voff)[_i]), (LAS unsigned*)(lds + (bufoff) + ldsw + _i * 8192), 16, 0, 0); } while (0)
; #define PG8_LDA(dst, b, h) do { _Pragma("unroll") for (int m = 0; m < 4; ++m) _Pragma("unroll") for (int k = 0; k < 2; ++k) dst[m][k] = *(const LAS bf16x8*)(lds + PG8_SA(b, h) + aoff + m * 2048 + k * 1024); } while (0)
; #define PG8_LDB(dst, b, h) do { _Pragma("unroll") for (int n = 0; n < 2; ++n) _Pragma("unroll") for (int k = 0; k < 2; ++k) dst[n][k] = *(const LAS bf16x8*)(lds + PG8_SB(b, h) + boff + n * 2048 + k * 1024); } while (0)
; #define PG8_MMA(ai, bj, At, Bt) do { __builtin_amdgcn_s_setprio(1); _Pragma("unroll") for (int m = 0; m < 4; ++m) _Pragma("unroll") for (int n = 0; n < 2; ++n) _Pragma("unroll") for (int k = 0; k < 2; ++k) \
;         acc[ai][bj][m][n] = __builtin_amdgcn_mfma_f32_16x16x32_bf16(Bt[n][k], At[m][k], acc[ai][bj][m][n], 0, 0, 0); __builtin_amdgcn_s_setprio(0); } while (0)
; #define PG8_WAIT_V(n) asm volatile("s_waitcnt vmcnt(" #n ")" ::: "memory")
; #define PG8_WAIT_L(n) asm volatile("s_waitcnt lgkmcnt(" #n ")" ::: "memory")
; #define PG8_BAR __builtin_amdgcn_s_barrier()
; #define PG8_SCHED __builtin_amdgcn_sched_barrier(0)
; #define PG8_STAGE(bufoff, gbase, voff) do { _Pragma("unroll") for (int _i = 0; _i < 2; ++_i) \
;         __builtin_amdgcn_global_load_lds((const unsigned*)((const char*)(gbase) + (voff)[_i]), (LAS unsigned*)(lds + (bufoff) + ldsw + _i * 8192), 16, 0, 0); } while (0)
; #define PG8_LDA(dst, b, h) do { _Pragma("unroll") for (int m = 0; m < 4; ++m) _Pragma("unroll") for (int k = 0; k < 2; ++k) dst[m][k] = *(const LAS bf16x8*)(lds + PG8_SA(b, h) + aoff + m * 2048 + k * 1024); } while (0)
;     ...
;             PG8_LDB(B0, 1, 0); PG8_LDB(B1, 1, 1); PG8_SCHED; PG8_LDA(At, 1, 0); PG8_STAGE(PG8_SA(0, 1), a2 + hstepA, voffA);
;             PG8_WAIT_V(8); PG8_WAIT_L(0); PG8_BAR; PG8_MMA(0, 0, At, B0); PG8_MMA(0, 1, At, B1); PG8_BAR; PG8_SCHED;
;             PG8_LDA(At, 1, 1); PG8_STAGE(PG8_SB(1, 0), b3, voffB); PG8_STAGE(PG8_SB(1, 1), b3 + hstep, voffB); PG8_STAGE(PG8_SA(1, 0), a3, voffA);
;             PG8_WAIT_V(8); PG8_WAIT_L(0); PG8_BAR; if (hi_on) { PG8_MMA(1, 0, At, B0); PG8_MMA(1, 1, At, B1); } PG8_BAR; PG8_SCHED;
;         }
	s_add_i32 s24, s27, s29
	v_lshl_add_u64 v[56:57], v[196:197], 0, s[88:89]
	s_mov_b32 m0, s24
	ds_read_b128 v[184:187], v166 offset:49152
	ds_read_b128 v[188:191], v166 offset:50176
	ds_read_b128 v[192:195], v166 offset:51200
	ds_read_b128 v[204:207], v166 offset:52224
	ds_read_b128 v[208:211], v166 offset:53248
	ds_read_b128 v[212:215], v166 offset:54272
	ds_read_b128 v[216:219], v166 offset:55296
	ds_read_b128 v[220:223], v166 offset:56320
	global_load_lds_dwordx4 v[56:57], off
	s_add_i32 m0, s24, 0x2000
	s_add_u32 s22, s22, 0x40080
	v_lshl_add_u64 v[56:57], v[224:225], 0, s[88:89]
	s_addc_u32 s23, s23, 0
	s_add_i32 s24, s36, s29
	global_load_lds_dwordx4 v[56:57], off
	v_lshl_add_u64 v[56:57], s[22:23], 0, v[144:145]
	s_mov_b32 m0, s24
	s_nop 0
	global_load_lds_dwordx4 v[56:57], off
	v_lshl_add_u64 v[56:57], s[22:23], 0, v[148:149]
	s_add_i32 m0, s24, 0x2000
	s_nop 0
	global_load_lds_dwordx4 v[56:57], off
	v_lshl_add_u64 v[56:57], v[226:227], 0, s[88:89]
	s_mov_b32 m0, s39
	s_nop 0
	global_load_lds_dwordx4 v[56:57], off
	v_lshl_add_u64 v[56:57], v[228:229], 0, s[88:89]
	s_mov_b32 m0, s40
	s_nop 0
	global_load_lds_dwordx4 v[56:57], off
	s_waitcnt vmcnt(8)
	s_waitcnt lgkmcnt(0)
	s_barrier
	s_setprio 1
	s_waitcnt lgkmcnt(0)
	v_mfma_f32_16x16x32_bf16 v[74:77], v[62:65], v[184:187], v[74:77]
	v_mfma_f32_16x16x32_bf16 v[70:73], v[156:159], v[184:187], v[70:73]
	v_mfma_f32_16x16x32_bf16 v[48:51], v[62:65], v[192:195], v[48:51]
	v_mfma_f32_16x16x32_bf16 v[44:47], v[156:159], v[192:195], v[44:47]
	v_mfma_f32_16x16x32_bf16 v[30:33], v[62:65], v[208:211], v[30:33]
	v_mfma_f32_16x16x32_bf16 v[26:29], v[156:159], v[208:211], v[26:29]
	v_mfma_f32_16x16x32_bf16 v[14:17], v[62:65], v[216:219], v[14:17]
	v_mfma_f32_16x16x32_bf16 v[10:13], v[156:159], v[216:219], v[10:13]
	v_mfma_f32_16x16x32_bf16 v[74:77], v[66:69], v[188:191], v[74:77]
	v_mfma_f32_16x16x32_bf16 v[70:73], v[160:163], v[188:191], v[70:73]
	v_mfma_f32_16x16x32_bf16 v[48:51], v[66:69], v[204:207], v[48:51]
	v_mfma_f32_16x16x32_bf16 v[44:47], v[160:163], v[204:207], v[44:47]
	v_mfma_f32_16x16x32_bf16 v[30:33], v[66:69], v[212:215], v[30:33]
	v_mfma_f32_16x16x32_bf16 v[26:29], v[160:163], v[212:215], v[26:29]
	v_mfma_f32_16x16x32_bf16 v[14:17], v[66:69], v[220:223], v[14:17]
	v_mfma_f32_16x16x32_bf16 v[10:13], v[160:163], v[220:223], v[10:13]
	v_mfma_f32_16x16x32_bf16 v[56:59], v[168:171], v[184:187], v[58:61]
	v_mfma_f32_16x16x32_bf16 v[52:55], v[176:179], v[184:187], v[52:55]
	v_mfma_f32_16x16x32_bf16 v[40:43], v[168:171], v[192:195], v[40:43]
	v_mfma_f32_16x16x32_bf16 v[36:39], v[176:179], v[192:195], v[36:39]
	v_mfma_f32_16x16x32_bf16 v[22:25], v[168:171], v[208:211], v[22:25]
	v_mfma_f32_16x16x32_bf16 v[18:21], v[176:179], v[208:211], v[18:21]
	v_mfma_f32_16x16x32_bf16 v[6:9], v[168:171], v[216:219], v[6:9]
	v_mfma_f32_16x16x32_bf16 v[2:5], v[176:179], v[216:219], v[2:5]
	v_mfma_f32_16x16x32_bf16 v[58:61], v[172:175], v[188:191], v[56:59]
	v_mfma_f32_16x16x32_bf16 v[54:57], v[180:183], v[188:191], v[52:55]
	v_mfma_f32_16x16x32_bf16 v[40:43], v[172:175], v[204:207], v[40:43]
	v_mfma_f32_16x16x32_bf16 v[36:39], v[180:183], v[204:207], v[36:39]
	v_mfma_f32_16x16x32_bf16 v[22:25], v[172:175], v[212:215], v[22:25]
	v_mfma_f32_16x16x32_bf16 v[18:21], v[180:183], v[212:215], v[18:21]
	v_mfma_f32_16x16x32_bf16 v[6:9], v[172:175], v[220:223], v[6:9]
	v_mfma_f32_16x16x32_bf16 v[2:5], v[180:183], v[220:223], v[2:5]
	s_setprio 0
	s_barrier
	s_add_i32 s26, s26, 2
	s_add_u32 s6, s6, 0x100
	s_addc_u32 s7, s7, 0
	s_add_u32 s15, s15, 0x100
	s_addc_u32 s17, s17, 0
	s_cmp_gt_u32 s26, 13
	s_cbranch_scc0 .LBB0_213
	s_and_b64 vcc, exec, s[12:13]
	s_cbranch_vccz .LBB0_216
	s_barrier

; #define PG8_STAGE(bufoff, gbase, voff) do { _Pragma("unroll") for (int _i = 0; _i < 2; ++_i) \
;         __builtin_amdgcn_global_load_lds((const unsigned*)((const char*)(gbase) + (voff)[_i]), (LAS unsigned*)(lds + (bufoff) + ldsw + _i * 8192), 16, 0, 0); } while (0)
; #define PG8_LDA(dst, b, h) do { _Pragma("unroll") for (int m = 0; m < 4; ++m) _Pragma("unroll") for (int k = 0; k < 2; ++k) dst[m][k] = *(const LAS bf16x8*)(lds + PG8_SA(b, h) + aoff + m * 2048 + k * 1024); } while (0)
; #define PG8_LDB(dst, b, h) do { _Pragma("unroll") for (int n = 0; n < 2; ++n) _Pragma("unroll") for (int k = 0; k < 2; ++k) dst[n][k] = *(const LAS bf16x8*)(lds + PG8_SB(b, h) + boff + n * 2048 + k * 1024); } while (0)
; #define PG8_MMA(ai, bj, At, Bt) do { __builtin_amdgcn_s_setprio(1); _Pragma("unroll") for (int m = 0; m < 4; ++m) _Pragma("unroll") for (int n = 0; n < 2; ++n) _Pragma("unroll") for (int k = 0; k < 2; ++k) \
;         acc[ai][bj][m][n] = __builtin_amdgcn_mfma_f32_16x16x32_bf16(Bt[n][k], At[m][k], acc[ai][bj][m][n], 0, 0, 0); __builtin_amdgcn_s_setprio(0); } while (0)
; #define PG8_WAIT_V(n) asm volatile("s_waitcnt vmcnt(" #n ")" ::: "memory")
; #define PG8_WAIT_L(n) asm volatile("s_waitcnt lgkmcnt(" #n ")" ::: "memory")
; #define PG8_BAR __builtin_amdgcn_s_barrier()
; #define PG8_SCHED __builtin_amdgcn_sched_barrier(0)
; #define PG8_STAGE(bufoff, gbase, voff) do { _Pragma("unroll") for (int _i = 0; _i < 2; ++_i) \
;         __builtin_amdgcn_global_load_lds((const unsigned*)((const char*)(gbase) + (voff)[_i]), (LAS unsigned*)(lds + (bufoff) + ldsw + _i * 8192), 16, 0, 0); } while (0)
; #define PG8_LDA(dst, b, h) do { _Pragma("unroll") for (int m = 0; m < 4; ++m) _Pragma("unroll") for (int k = 0; k < 2; ++k) dst[m][k] = *(const LAS bf16x8*)(lds + PG8_SA(b, h) + aoff + m * 2048 + k * 1024); } while (0)
;     ...
;             PG8_LDB(B0, 0, 0); PG8_LDB(B1, 0, 1); PG8_SCHED; PG8_LDA(At, 0, 0); PG8_STAGE(PG8_SA(1, 1), a1 + hstepA, voffA);
;             PG8_WAIT_V(8); PG8_WAIT_L(0); PG8_BAR; PG8_MMA(0, 0, At, B0); PG8_MMA(0, 1, At, B1); PG8_BAR; PG8_SCHED;
;             PG8_LDA(At, 0, 1); PG8_STAGE(PG8_SB(0, 0), b2, voffB); PG8_STAGE(PG8_SB(0, 1), b2 + hstep, voffB); PG8_STAGE(PG8_SA(0, 0), a2, voffA);
;             PG8_WAIT_V(8); PG8_WAIT_L(0); PG8_BAR; if (hi_on) { PG8_MMA(1, 0, At, B0); PG8_MMA(1, 1, At, B1); } PG8_BAR; PG8_SCHED;
.LBB0_717:
	s_add_u32 s24, s22, 0x3fc000
	s_addc_u32 s25, s23, 0
	s_cmp_eq_u32 s45, 12
	s_cselect_b32 s28, s18, s24
	s_cselect_b32 s29, s19, s25
	s_cselect_b32 s26, s20, s15
	s_cselect_b32 s27, s21, s17
	s_add_u32 s24, s28, 0x400000
	s_addc_u32 s25, s29, 0
	s_add_i32 s33, 0, 0x10000
	s_add_i32 s48, 0, 0x14000
	v_add_u32_e32 v64, s33, v200
	v_add_u32_e32 v160, s48, v200
	ds_read_b128 v[52:55], v64
	ds_read_b128 v[56:59], v64 offset:1024
	ds_read_b128 v[60:63], v64 offset:2048
	ds_read_b128 v[64:67], v64 offset:3072
	ds_read_b128 v[148:151], v160
	ds_read_b128 v[152:155], v160 offset:1024
	ds_read_b128 v[156:159], v160 offset:2048
	ds_read_b128 v[160:163], v160 offset:3072
	v_lshl_add_u64 v[212:213], s[22:23], 0, v[194:195]
	s_add_i32 m0, s34, 0xc000
	ds_read_b128 v[164:167], v249
	ds_read_b128 v[168:171], v249 offset:1024
	ds_read_b128 v[172:175], v249 offset:2048
	ds_read_b128 v[176:179], v249 offset:3072
	ds_read_b128 v[180:183], v249 offset:4096
	ds_read_b128 v[184:187], v249 offset:5120
	ds_read_b128 v[204:207], v249 offset:6144
	ds_read_b128 v[208:211], v249 offset:7168
	global_load_lds_dwordx4 v[212:213], off
	v_lshl_add_u64 v[212:213], s[22:23], 0, v[196:197]
	s_add_i32 m0, s34, 0xe000
	s_nop 0
	global_load_lds_dwordx4 v[212:213], off
	s_waitcnt vmcnt(8)
	s_waitcnt lgkmcnt(0)
	s_barrier
	s_setprio 1
	s_waitcnt lgkmcnt(0)
	v_mfma_f32_16x16x32_bf16 v[144:147], v[52:55], v[164:167], v[144:147]
	v_mfma_f32_16x16x32_bf16 v[140:143], v[60:63], v[164:167], v[140:143]
	v_mfma_f32_16x16x32_bf16 v[128:131], v[52:55], v[172:175], v[128:131]
	v_mfma_f32_16x16x32_bf16 v[124:127], v[60:63], v[172:175], v[124:127]
	v_mfma_f32_16x16x32_bf16 v[112:115], v[52:55], v[180:183], v[112:115]
	v_mfma_f32_16x16x32_bf16 v[108:111], v[60:63], v[180:183], v[108:111]
	v_mfma_f32_16x16x32_bf16 v[96:99], v[52:55], v[204:207], v[96:99]
	v_mfma_f32_16x16x32_bf16 v[92:95], v[60:63], v[204:207], v[92:95]
	v_mfma_f32_16x16x32_bf16 v[144:147], v[56:59], v[168:171], v[144:147]
	v_mfma_f32_16x16x32_bf16 v[140:143], v[64:67], v[168:171], v[140:143]
	v_mfma_f32_16x16x32_bf16 v[128:131], v[56:59], v[176:179], v[128:131]
	v_mfma_f32_16x16x32_bf16 v[124:127], v[64:67], v[176:179], v[124:127]
	v_mfma_f32_16x16x32_bf16 v[112:115], v[56:59], v[184:187], v[112:115]
	v_mfma_f32_16x16x32_bf16 v[108:111], v[64:67], v[184:187], v[108:111]
	v_mfma_f32_16x16x32_bf16 v[96:99], v[56:59], v[208:211], v[96:99]
	v_mfma_f32_16x16x32_bf16 v[92:95], v[64:67], v[208:211], v[92:95]
	v_mfma_f32_16x16x32_bf16 v[136:139], v[148:151], v[164:167], v[136:139]
	v_mfma_f32_16x16x32_bf16 v[132:135], v[156:159], v[164:167], v[132:135]
	v_mfma_f32_16x16x32_bf16 v[120:123], v[148:151], v[172:175], v[120:123]
	v_mfma_f32_16x16x32_bf16 v[116:119], v[156:159], v[172:175], v[116:119]
	v_mfma_f32_16x16x32_bf16 v[104:107], v[148:151], v[180:183], v[104:107]
	v_mfma_f32_16x16x32_bf16 v[100:103], v[156:159], v[180:183], v[100:103]
	v_mfma_f32_16x16x32_bf16 v[88:91], v[148:151], v[204:207], v[88:91]
	v_mfma_f32_16x16x32_bf16 v[84:87], v[156:159], v[204:207], v[84:87]
	v_mfma_f32_16x16x32_bf16 v[136:139], v[152:155], v[168:171], v[136:139]
	v_mfma_f32_16x16x32_bf16 v[132:135], v[160:163], v[168:171], v[132:135]
	v_mfma_f32_16x16x32_bf16 v[120:123], v[152:155], v[176:179], v[120:123]
	v_mfma_f32_16x16x32_bf16 v[116:119], v[160:163], v[176:179], v[116:119]
	v_mfma_f32_16x16x32_bf16 v[104:107], v[152:155], v[184:187], v[104:107]
	v_mfma_f32_16x16x32_bf16 v[100:103], v[160:163], v[184:187], v[100:103]
	v_mfma_f32_16x16x32_bf16 v[88:91], v[152:155], v[208:211], v[88:91]
	v_mfma_f32_16x16x32_bf16 v[84:87], v[160:163], v[208:211], v[84:87]
	s_setprio 0
	s_barrier
	s_add_i32 s33, s33, s31
	v_lshl_add_u64 v[212:213], s[26:27], 0, v[34:35]
	s_mov_b32 m0, s33
	ds_read_b128 v[164:167], v249 offset:16384
	ds_read_b128 v[168:171], v249 offset:17408
	ds_read_b128 v[172:175], v249 offset:18432
	ds_read_b128 v[176:179], v249 offset:19456
	ds_read_b128 v[180:183], v249 offset:20480
	ds_read_b128 v[184:187], v249 offset:21504
	ds_read_b128 v[204:207], v249 offset:22528
	ds_read_b128 v[208:211], v249 offset:23552
	global_load_lds_dwordx4 v[212:213], off
	s_add_i32 m0, s33, 0x2000
	s_add_u32 s46, s26, 0x40000
	v_lshl_add_u64 v[214:215], s[26:27], 0, v[188:189]
	s_addc_u32 s47, s27, 0
	s_add_i32 s33, s48, s31
	global_load_lds_dwordx4 v[214:215], off
	v_lshl_add_u64 v[216:217], s[46:47], 0, v[34:35]
	s_mov_b32 m0, s33
	s_nop 0
	global_load_lds_dwordx4 v[216:217], off
	v_lshl_add_u64 v[216:217], s[46:47], 0, v[188:189]
	s_add_i32 m0, s33, 0x2000
	s_nop 0
	global_load_lds_dwordx4 v[216:217], off
	v_lshl_add_u64 v[216:217], s[28:29], 0, v[192:193]
	s_mov_b32 m0, s34
	s_nop 0
	global_load_lds_dwordx4 v[216:217], off
	v_lshl_add_u64 v[216:217], s[28:29], 0, v[190:191]
	s_mov_b32 m0, s35
	s_nop 0
	global_load_lds_dwordx4 v[216:217], off
	s_waitcnt vmcnt(8)
	s_waitcnt lgkmcnt(0)
	s_barrier
; #define PG8_STAGE(bufoff, gbase, voff) do { _Pragma("unroll") for (int _i = 0; _i < 2; ++_i) \
;         __builtin_amdgcn_global_load_lds((const unsigned*)((const char*)(gbase) + (voff)[_i]), (LAS unsigned*)(lds + (bufoff) + ldsw + _i * 8192), 16, 0, 0); } while (0)
; #define PG8_LDA(dst, b, h) do { _Pragma("unroll") for (int m = 0; m < 4; ++m) _Pragma("unroll") for (int k = 0; k < 2; ++k) dst[m][k] = *(const LAS bf16x8*)(lds + PG8_SA(b, h) + aoff + m * 2048 + k * 1024); } while (0)
; #define PG8_LDB(dst, b, h) do { _Pragma("unroll") for (int n = 0; n < 2; ++n) _Pragma("unroll") for (int k = 0; k < 2; ++k) dst[n][k] = *(const LAS bf16x8*)(lds + PG8_SB(b, h) + boff + n * 2048 + k * 1024); } while (0)
; #define PG8_MMA(ai, bj, At, Bt) do { __builtin_amdgcn_s_setprio(1); _Pragma("unroll") for (int m = 0; m < 4; ++m) _Pragma("unroll") for (int n = 0; n < 2; ++n) _Pragma("unroll") for (int k = 0; k < 2; ++k) \
;         acc[ai][bj][m][n] = __builtin_amdgcn_mfma_f32_16x16x32_bf16(Bt[n][k], At[m][k], acc[ai][bj][m][n], 0, 0, 0); __builtin_amdgcn_s_setprio(0); } while (0)
; #define PG8_WAIT_V(n) asm volatile("s_waitcnt vmcnt(" #n ")" ::: "memory")
; #define PG8_WAIT_L(n) asm volatile("s_waitcnt lgkmcnt(" #n ")" ::: "memory")
; #define PG8_BAR __builtin_amdgcn_s_barrier()
; #define PG8_SCHED __builtin_amdgcn_sched_barrier(0)
; #define PG8_STAGE(bufoff, gbase, voff) do { _Pragma("unroll") for (int _i = 0; _i < 2; ++_i) \
;         __builtin_amdgcn_global_load_lds((const unsigned*)((const char*)(gbase) + (voff)[_i]), (LAS unsigned*)(lds + (bufoff) + ldsw + _i * 8192), 16, 0, 0); } while (0)
; #define PG8_LDA(dst, b, h) do { _Pragma("unroll") for (int m = 0; m < 4; ++m) _Pragma("unroll") for (int k = 0; k < 2; ++k) dst[m][k] = *(const LAS bf16x8*)(lds + PG8_SA(b, h) + aoff + m * 2048 + k * 1024); } while (0)
;     ...
;             PG8_LDA(At, 0, 1); PG8_STAGE(PG8_SB(0, 0), b2, voffB); PG8_STAGE(PG8_SB(0, 1), b2 + hstep, voffB); PG8_STAGE(PG8_SA(0, 0), a2, voffA);
;             PG8_WAIT_V(8); PG8_WAIT_L(0); PG8_BAR; if (hi_on) { PG8_MMA(1, 0, At, B0); PG8_MMA(1, 1, At, B1); } PG8_BAR; PG8_SCHED;
;             PG8_LDB(B0, 1, 0); PG8_LDB(B1, 1, 1); PG8_SCHED; PG8_LDA(At, 1, 0); PG8_STAGE(PG8_SA(0, 1), a2 + hstepA, voffA);
;             PG8_WAIT_V(8); PG8_WAIT_L(0); PG8_BAR; PG8_MMA(0, 0, At, B0); PG8_MMA(0, 1, At, B1); PG8_BAR; PG8_SCHED;
	s_setprio 1
	s_waitcnt lgkmcnt(0)
	v_mfma_f32_16x16x32_bf16 v[80:83], v[52:55], v[164:167], v[80:83]
	v_mfma_f32_16x16x32_bf16 v[76:79], v[60:63], v[164:167], v[76:79]
	v_mfma_f32_16x16x32_bf16 v[48:51], v[52:55], v[172:175], v[48:51]
	v_mfma_f32_16x16x32_bf16 v[44:47], v[60:63], v[172:175], v[44:47]
	v_mfma_f32_16x16x32_bf16 v[30:33], v[52:55], v[180:183], v[30:33]
	v_mfma_f32_16x16x32_bf16 v[26:29], v[60:63], v[180:183], v[26:29]
	v_mfma_f32_16x16x32_bf16 v[14:17], v[52:55], v[204:207], v[14:17]
	v_mfma_f32_16x16x32_bf16 v[10:13], v[60:63], v[204:207], v[10:13]
	v_mfma_f32_16x16x32_bf16 v[80:83], v[56:59], v[168:171], v[80:83]
	v_mfma_f32_16x16x32_bf16 v[76:79], v[64:67], v[168:171], v[76:79]
	v_mfma_f32_16x16x32_bf16 v[48:51], v[56:59], v[176:179], v[48:51]
	v_mfma_f32_16x16x32_bf16 v[44:47], v[64:67], v[176:179], v[44:47]
	v_mfma_f32_16x16x32_bf16 v[30:33], v[56:59], v[184:187], v[30:33]
	v_mfma_f32_16x16x32_bf16 v[26:29], v[64:67], v[184:187], v[26:29]
	v_mfma_f32_16x16x32_bf16 v[14:17], v[56:59], v[208:211], v[14:17]
	v_mfma_f32_16x16x32_bf16 v[10:13], v[64:67], v[208:211], v[10:13]
	v_mfma_f32_16x16x32_bf16 v[40:43], v[148:151], v[172:175], v[40:43]
	v_mfma_f32_16x16x32_bf16 v[36:39], v[156:159], v[172:175], v[36:39]
	v_mfma_f32_16x16x32_bf16 v[22:25], v[148:151], v[180:183], v[22:25]
	v_mfma_f32_16x16x32_bf16 v[18:21], v[156:159], v[180:183], v[18:21]
	v_mfma_f32_16x16x32_bf16 v[6:9], v[148:151], v[204:207], v[6:9]
	v_mfma_f32_16x16x32_bf16 v[2:5], v[156:159], v[204:207], v[2:5]
	v_mfma_f32_16x16x32_bf16 v[52:55], v[148:151], v[164:167], v[72:75]
	v_mfma_f32_16x16x32_bf16 v[56:59], v[156:159], v[164:167], v[68:71]
	v_mfma_f32_16x16x32_bf16 v[40:43], v[152:155], v[176:179], v[40:43]
	v_mfma_f32_16x16x32_bf16 v[36:39], v[160:163], v[176:179], v[36:39]
	v_mfma_f32_16x16x32_bf16 v[22:25], v[152:155], v[184:187], v[22:25]
	v_mfma_f32_16x16x32_bf16 v[18:21], v[160:163], v[184:187], v[18:21]
	v_mfma_f32_16x16x32_bf16 v[6:9], v[152:155], v[208:211], v[6:9]
	v_mfma_f32_16x16x32_bf16 v[2:5], v[160:163], v[208:211], v[2:5]
	v_mfma_f32_16x16x32_bf16 v[52:55], v[152:155], v[168:171], v[52:55]
	v_mfma_f32_16x16x32_bf16 v[56:59], v[160:163], v[168:171], v[56:59]
	s_setprio 0
	s_barrier
	s_add_i32 s33, 0, 0x18000
	s_add_i32 s46, 0, 0x1c000
	v_add_u32_e32 v72, s33, v200
	v_add_u32_e32 v160, s46, v200
	ds_read_b128 v[60:63], v72
	ds_read_b128 v[64:67], v72 offset:1024
	ds_read_b128 v[68:71], v72 offset:2048
	ds_read_b128 v[72:75], v72 offset:3072
	ds_read_b128 v[148:151], v160
	ds_read_b128 v[152:155], v160 offset:1024
	ds_read_b128 v[156:159], v160 offset:2048
	ds_read_b128 v[160:163], v160 offset:3072
	s_add_u32 s28, s28, 0x4000
	s_addc_u32 s29, s29, 0
	s_mov_b32 m0, s38
	v_lshl_add_u64 v[216:217], s[28:29], 0, v[192:193]
	ds_read_b128 v[164:167], v249 offset:32768
	ds_read_b128 v[168:171], v249 offset:33792
	ds_read_b128 v[172:175], v249 offset:34816
	ds_read_b128 v[176:179], v249 offset:35840
	ds_read_b128 v[180:183], v249 offset:36864
	ds_read_b128 v[184:187], v249 offset:37888
	ds_read_b128 v[204:207], v249 offset:38912
	ds_read_b128 v[208:211], v249 offset:39936
	global_load_lds_dwordx4 v[216:217], off
	v_lshl_add_u64 v[216:217], s[28:29], 0, v[190:191]
	s_mov_b32 m0, s39
	s_nop 0
	global_load_lds_dwordx4 v[216:217], off
	s_waitcnt vmcnt(8)
	s_waitcnt lgkmcnt(0)
	s_barrier
	s_setprio 1
	s_waitcnt lgkmcnt(0)
	v_mfma_f32_16x16x32_bf16 v[144:147], v[60:63], v[164:167], v[144:147]
	v_mfma_f32_16x16x32_bf16 v[140:143], v[68:71], v[164:167], v[140:143]
	v_mfma_f32_16x16x32_bf16 v[128:131], v[60:63], v[172:175], v[128:131]
	v_mfma_f32_16x16x32_bf16 v[124:127], v[68:71], v[172:175], v[124:127]
	v_mfma_f32_16x16x32_bf16 v[112:115], v[60:63], v[180:183], v[112:115]
	v_mfma_f32_16x16x32_bf16 v[108:111], v[68:71], v[180:183], v[108:111]
	v_mfma_f32_16x16x32_bf16 v[96:99], v[60:63], v[204:207], v[96:99]
	v_mfma_f32_16x16x32_bf16 v[92:95], v[68:71], v[204:207], v[92:95]
	v_mfma_f32_16x16x32_bf16 v[144:147], v[64:67], v[168:171], v[144:147]
	v_mfma_f32_16x16x32_bf16 v[140:143], v[72:75], v[168:171], v[140:143]
	v_mfma_f32_16x16x32_bf16 v[128:131], v[64:67], v[176:179], v[128:131]
	v_mfma_f32_16x16x32_bf16 v[124:127], v[72:75], v[176:179], v[124:127]
	v_mfma_f32_16x16x32_bf16 v[112:115], v[64:67], v[184:187], v[112:115]
	v_mfma_f32_16x16x32_bf16 v[108:111], v[72:75], v[184:187], v[108:111]
	v_mfma_f32_16x16x32_bf16 v[96:99], v[64:67], v[208:211], v[96:99]
	v_mfma_f32_16x16x32_bf16 v[92:95], v[72:75], v[208:211], v[92:95]
	v_mfma_f32_16x16x32_bf16 v[136:139], v[148:151], v[164:167], v[136:139]
	v_mfma_f32_16x16x32_bf16 v[132:135], v[156:159], v[164:167], v[132:135]
	v_mfma_f32_16x16x32_bf16 v[120:123], v[148:151], v[172:175], v[120:123]
	v_mfma_f32_16x16x32_bf16 v[116:119], v[156:159], v[172:175], v[116:119]
	v_mfma_f32_16x16x32_bf16 v[104:107], v[148:151], v[180:183], v[104:107]
	v_mfma_f32_16x16x32_bf16 v[100:103], v[156:159], v[180:183], v[100:103]
	v_mfma_f32_16x16x32_bf16 v[88:91], v[148:151], v[204:207], v[88:91]
	v_mfma_f32_16x16x32_bf16 v[84:87], v[156:159], v[204:207], v[84:87]
	v_mfma_f32_16x16x32_bf16 v[136:139], v[152:155], v[168:171], v[136:139]
	v_mfma_f32_16x16x32_bf16 v[132:135], v[160:163], v[168:171], v[132:135]
	v_mfma_f32_16x16x32_bf16 v[120:123], v[152:155], v[176:179], v[120:123]
	v_mfma_f32_16x16x32_bf16 v[116:119], v[160:163], v[176:179], v[116:119]
	v_mfma_f32_16x16x32_bf16 v[104:107], v[152:155], v[184:187], v[104:107]
	v_mfma_f32_16x16x32_bf16 v[100:103], v[160:163], v[184:187], v[100:103]
	v_mfma_f32_16x16x32_bf16 v[88:91], v[152:155], v[208:211], v[88:91]
	v_mfma_f32_16x16x32_bf16 v[84:87], v[160:163], v[208:211], v[84:87]
	s_setprio 0
	s_barrier
; #define PG8_STAGE(bufoff, gbase, voff) do { _Pragma("unroll") for (int _i = 0; _i < 2; ++_i) \
;         __builtin_amdgcn_global_load_lds((const unsigned*)((const char*)(gbase) + (voff)[_i]), (LAS unsigned*)(lds + (bufoff) + ldsw + _i * 8192), 16, 0, 0); } while (0)
; #define PG8_LDA(dst, b, h) do { _Pragma("unroll") for (int m = 0; m < 4; ++m) _Pragma("unroll") for (int k = 0; k < 2; ++k) dst[m][k] = *(const LAS bf16x8*)(lds + PG8_SA(b, h) + aoff + m * 2048 + k * 1024); } while (0)
; #define PG8_LDB(dst, b, h) do { _Pragma("unroll") for (int n = 0; n < 2; ++n) _Pragma("unroll") for (int k = 0; k < 2; ++k) dst[n][k] = *(const LAS bf16x8*)(lds + PG8_SB(b, h) + boff + n * 2048 + k * 1024); } while (0)
; #define PG8_MMA(ai, bj, At, Bt) do { __builtin_amdgcn_s_setprio(1); _Pragma("unroll") for (int m = 0; m < 4; ++m) _Pragma("unroll") for (int n = 0; n < 2; ++n) _Pragma("unroll") for (int k = 0; k < 2; ++k) \
;         acc[ai][bj][m][n] = __builtin_amdgcn_mfma_f32_16x16x32_bf16(Bt[n][k], At[m][k], acc[ai][bj][m][n], 0, 0, 0); __builtin_amdgcn_s_setprio(0); } while (0)
; #define PG8_WAIT_V(n) asm volatile("s_waitcnt vmcnt(" #n ")" ::: "memory")
; #define PG8_WAIT_L(n) asm volatile("s_waitcnt lgkmcnt(" #n ")" ::: "memory")
; #define PG8_BAR __builtin_amdgcn_s_barrier()
; #define PG8_SCHED __builtin_amdgcn_sched_barrier(0)
; #define PG8_STAGE(bufoff, gbase, voff) do { _Pragma("unroll") for (int _i = 0; _i < 2; ++_i) \
;         __builtin_amdgcn_global_load_lds((const unsigned*)((const char*)(gbase) + (voff)[_i]), (LAS unsigned*)(lds + (bufoff) + ldsw + _i * 8192), 16, 0, 0); } while (0)
; #define PG8_LDA(dst, b, h) do { _Pragma("unroll") for (int m = 0; m < 4; ++m) _Pragma("unroll") for (int k = 0; k < 2; ++k) dst[m][k] = *(const LAS bf16x8*)(lds + PG8_SA(b, h) + aoff + m * 2048 + k * 1024); } while (0)
;     ...
;             PG8_LDB(B0, 1, 0); PG8_LDB(B1, 1, 1); PG8_SCHED; PG8_LDA(At, 1, 0); PG8_STAGE(PG8_SA(0, 1), a2 + hstepA, voffA);
;             PG8_WAIT_V(8); PG8_WAIT_L(0); PG8_BAR; PG8_MMA(0, 0, At, B0); PG8_MMA(0, 1, At, B1); PG8_BAR; PG8_SCHED;
;             PG8_LDA(At, 1, 1); PG8_STAGE(PG8_SB(1, 0), b3, voffB); PG8_STAGE(PG8_SB(1, 1), b3 + hstep, voffB); PG8_STAGE(PG8_SA(1, 0), a3, voffA);
;             PG8_WAIT_V(8); PG8_WAIT_L(0); PG8_BAR; if (hi_on) { PG8_MMA(1, 0, At, B0); PG8_MMA(1, 1, At, B1); } PG8_BAR; PG8_SCHED;
;         }
	s_add_i32 s28, s33, s31
	v_lshl_add_u64 v[212:213], v[212:213], 0, s[88:89]
	s_mov_b32 m0, s28
	ds_read_b128 v[164:167], v249 offset:49152
	ds_read_b128 v[168:171], v249 offset:50176
	ds_read_b128 v[172:175], v249 offset:51200
	ds_read_b128 v[176:179], v249 offset:52224
	ds_read_b128 v[180:183], v249 offset:53248
	ds_read_b128 v[184:187], v249 offset:54272
	ds_read_b128 v[204:207], v249 offset:55296
	ds_read_b128 v[208:211], v249 offset:56320
	global_load_lds_dwordx4 v[212:213], off
	s_add_i32 m0, s28, 0x2000
	s_add_u32 s26, s26, 0x40080
	v_lshl_add_u64 v[212:213], v[214:215], 0, s[88:89]
	s_addc_u32 s27, s27, 0
	s_add_i32 s28, s46, s31
	global_load_lds_dwordx4 v[212:213], off
	v_lshl_add_u64 v[212:213], s[26:27], 0, v[34:35]
	s_mov_b32 m0, s28
	s_nop 0
	global_load_lds_dwordx4 v[212:213], off
	v_lshl_add_u64 v[212:213], s[26:27], 0, v[188:189]
	s_add_i32 m0, s28, 0x2000
	s_nop 0
	global_load_lds_dwordx4 v[212:213], off
	v_lshl_add_u64 v[212:213], s[24:25], 0, v[192:193]
	s_mov_b32 m0, s41
	s_nop 0
	global_load_lds_dwordx4 v[212:213], off
	v_lshl_add_u64 v[212:213], s[24:25], 0, v[190:191]
	s_mov_b32 m0, s42
	s_nop 0
	global_load_lds_dwordx4 v[212:213], off
	s_waitcnt vmcnt(8)
	s_waitcnt lgkmcnt(0)
	s_barrier
	s_setprio 1
	s_waitcnt lgkmcnt(0)
	v_mfma_f32_16x16x32_bf16 v[80:83], v[60:63], v[164:167], v[80:83]
	v_mfma_f32_16x16x32_bf16 v[76:79], v[68:71], v[164:167], v[76:79]
	v_mfma_f32_16x16x32_bf16 v[48:51], v[60:63], v[172:175], v[48:51]
	v_mfma_f32_16x16x32_bf16 v[44:47], v[68:71], v[172:175], v[44:47]
	v_mfma_f32_16x16x32_bf16 v[30:33], v[60:63], v[180:183], v[30:33]
	v_mfma_f32_16x16x32_bf16 v[26:29], v[68:71], v[180:183], v[26:29]
	v_mfma_f32_16x16x32_bf16 v[14:17], v[60:63], v[204:207], v[14:17]
	v_mfma_f32_16x16x32_bf16 v[10:13], v[68:71], v[204:207], v[10:13]
	v_mfma_f32_16x16x32_bf16 v[80:83], v[64:67], v[168:171], v[80:83]
	v_mfma_f32_16x16x32_bf16 v[76:79], v[72:75], v[168:171], v[76:79]
	v_mfma_f32_16x16x32_bf16 v[48:51], v[64:67], v[176:179], v[48:51]
	v_mfma_f32_16x16x32_bf16 v[44:47], v[72:75], v[176:179], v[44:47]
	v_mfma_f32_16x16x32_bf16 v[30:33], v[64:67], v[184:187], v[30:33]
	v_mfma_f32_16x16x32_bf16 v[26:29], v[72:75], v[184:187], v[26:29]
	v_mfma_f32_16x16x32_bf16 v[14:17], v[64:67], v[208:211], v[14:17]
	v_mfma_f32_16x16x32_bf16 v[10:13], v[72:75], v[208:211], v[10:13]
	v_mfma_f32_16x16x32_bf16 v[52:55], v[148:151], v[164:167], v[52:55]
	v_mfma_f32_16x16x32_bf16 v[72:75], v[152:155], v[168:171], v[52:55]
	v_mfma_f32_16x16x32_bf16 v[52:55], v[156:159], v[164:167], v[56:59]
	v_mfma_f32_16x16x32_bf16 v[40:43], v[148:151], v[172:175], v[40:43]
	v_mfma_f32_16x16x32_bf16 v[36:39], v[156:159], v[172:175], v[36:39]
	v_mfma_f32_16x16x32_bf16 v[22:25], v[148:151], v[180:183], v[22:25]
	v_mfma_f32_16x16x32_bf16 v[18:21], v[156:159], v[180:183], v[18:21]
	v_mfma_f32_16x16x32_bf16 v[6:9], v[148:151], v[204:207], v[6:9]
	v_mfma_f32_16x16x32_bf16 v[2:5], v[156:159], v[204:207], v[2:5]
	v_mfma_f32_16x16x32_bf16 v[68:71], v[160:163], v[168:171], v[52:55]
	v_mfma_f32_16x16x32_bf16 v[40:43], v[152:155], v[176:179], v[40:43]
	v_mfma_f32_16x16x32_bf16 v[36:39], v[160:163], v[176:179], v[36:39]
	v_mfma_f32_16x16x32_bf16 v[22:25], v[152:155], v[184:187], v[22:25]
	v_mfma_f32_16x16x32_bf16 v[18:21], v[160:163], v[184:187], v[18:21]
	v_mfma_f32_16x16x32_bf16 v[6:9], v[152:155], v[208:211], v[6:9]
	v_mfma_f32_16x16x32_bf16 v[2:5], v[160:163], v[208:211], v[2:5]
	s_setprio 0
	s_barrier
	s_add_i32 s45, s45, 2
	s_add_u32 s15, s15, 0x100
	s_addc_u32 s17, s17, 0
	s_add_u32 s22, s22, 0x800000
	s_addc_u32 s23, s23, 0
	s_cmp_gt_u32 s45, 13
	s_cbranch_scc0 .LBB0_717
	s_and_b64 vcc, exec, s[10:11]
	s_cbranch_vccz .LBB0_720
	s_barrier

; #define PG8_STAGE(bufoff, gbase, voff) do { _Pragma("unroll") for (int _i = 0; _i < 2; ++_i) \
;         __builtin_amdgcn_global_load_lds((const unsigned*)((const char*)(gbase) + (voff)[_i]), (LAS unsigned*)(lds + (bufoff) + ldsw + _i * 8192), 16, 0, 0); } while (0)
; #define PG8_LDA(dst, b, h) do { _Pragma("unroll") for (int m = 0; m < 4; ++m) _Pragma("unroll") for (int k = 0; k < 2; ++k) dst[m][k] = *(const LAS bf16x8*)(lds + PG8_SA(b, h) + aoff + m * 2048 + k * 1024); } while (0)
; #define PG8_LDB(dst, b, h) do { _Pragma("unroll") for (int n = 0; n < 2; ++n) _Pragma("unroll") for (int k = 0; k < 2; ++k) dst[n][k] = *(const LAS bf16x8*)(lds + PG8_SB(b, h) + boff + n * 2048 + k * 1024); } while (0)
; #define PG8_MMA(ai, bj, At, Bt) do { __builtin_amdgcn_s_setprio(1); _Pragma("unroll") for (int m = 0; m < 4; ++m) _Pragma("unroll") for (int n = 0; n < 2; ++n) _Pragma("unroll") for (int k = 0; k < 2; ++k) \
;         acc[ai][bj][m][n] = __builtin_amdgcn_mfma_f32_16x16x32_bf16(Bt[n][k], At[m][k], acc[ai][bj][m][n], 0, 0, 0); __builtin_amdgcn_s_setprio(0); } while (0)
; #define PG8_BAR __builtin_amdgcn_s_barrier()
; template <class Epi, class Sched>
; __device__ __forceinline__ void gemm_phase_gather(LAS unsigned char* lds, const int K, const Sched& S, const Epi& E, const char* Ag, const int* list, const LAS int* seg) {
;     ...
;         for (int t = 0; t < nt; t += 2) {
;             const bool last = (t == nt - 2);
;             const char* a1 = cA + (size_t)(t + 1) * kstep;
;             const char* a2 = last ? cA : cA + (size_t)(t + 2) * kstep; const char* b2 = last ? nB : cB + (size_t)(t + 2) * kstep;
;             unsigned x0[2], x1[2];
;             x0[0] = last ? na0[0] : ca0[0]; x0[1] = last ? na0[1] : ca0[1]; x1[0] = last ? na1[0] : ca1[0]; x1[1] = last ? na1[1] : ca1[1];
;             const char* a3 = a2 + kstep; const char* b3 = b2 + kstep;
;             PG8_LDB(B0, 0, 0); PG8_LDB(B1, 0, 1); PG8_SCHED; PG8_LDA(At, 0, 0); PG8_STAGE(PG8_SA(1, 1), a1, ca1);
;             PG8_WAIT_V(8); PG8_WAIT_L(0); PG8_BAR; PG8_MMA(0, 0, At, B0); PG8_MMA(0, 1, At, B1); PG8_BAR; PG8_SCHED;
;             PG8_LDA(At, 0, 1); PG8_STAGE(PG8_SB(0, 0), b2, voffB); PG8_STAGE(PG8_SB(0, 1), b2 + hstep, voffB); PG8_STAGE(PG8_SA(0, 0), a2, x0);
;             PG8_WAIT_V(8); PG8_WAIT_L(0); PG8_BAR; if (hi_on) { PG8_MMA(1, 0, At, B0); PG8_MMA(1, 1, At, B1); } PG8_BAR; PG8_SCHED;
.LBB0_1035:
	s_add_u32 s6, s92, s36
	s_addc_u32 s7, s93, s37
	s_add_u32 s33, s6, 0x7c00100
	s_addc_u32 s38, s7, 0
	s_add_u32 s58, s54, s36
	s_addc_u32 s39, s55, s37
	s_add_i32 s59, 0, 0x10000
	s_cmpk_eq_i32 s36, 0x700
	s_cselect_b64 s[6:7], -1, 0
	s_and_b64 s[8:9], s[6:7], exec
	s_cselect_b32 s41, s81, s38
	s_cselect_b32 s40, s80, s33
	s_cselect_b32 s39, s75, s39
	s_cselect_b32 s38, s78, s58
	s_add_i32 s33, 0, 0x14000
	v_add_u32_e32 v134, s59, v248
	v_add_u32_e32 v146, s33, v248
	ds_read_b128 v[150:153], v134
	ds_read_b128 v[154:157], v134 offset:1024
	ds_read_b128 v[158:161], v134 offset:2048
	ds_read_b128 v[162:165], v134 offset:3072
	ds_read_b128 v[134:137], v146
	ds_read_b128 v[138:141], v146 offset:1024
	ds_read_b128 v[142:145], v146 offset:2048
	ds_read_b128 v[146:149], v146 offset:3072
	v_cndmask_b32_e64 v34, v209, v228, s[6:7]
	v_cndmask_b32_e64 v222, v212, v246, s[6:7]
	v_lshl_add_u64 v[218:219], v[216:217], 0, s[36:37]
	s_add_i32 m0, s15, 0xc000
	s_waitcnt lgkmcnt(0)
	ds_read_b128 v[166:169], v213
	ds_read_b128 v[170:173], v213 offset:1024
	ds_read_b128 v[174:177], v213 offset:2048
	ds_read_b128 v[178:181], v213 offset:3072
	ds_read_b128 v[182:185], v213 offset:4096
	ds_read_b128 v[186:189], v213 offset:5120
	ds_read_b128 v[190:193], v213 offset:6144
	ds_read_b128 v[194:197], v213 offset:7168
	global_load_lds_dwordx4 v[218:219], off
	v_lshl_add_u64 v[218:219], v[36:37], 0, s[36:37]
	s_add_i32 m0, s15, 0xe000
	s_nop 0
	global_load_lds_dwordx4 v[218:219], off
	s_waitcnt vmcnt(8)
	s_waitcnt lgkmcnt(0)
	s_barrier
	s_setprio 1
	s_waitcnt lgkmcnt(0)
	v_mfma_f32_16x16x32_bf16 v[74:77], v[150:153], v[166:169], v[74:77]
	v_mfma_f32_16x16x32_bf16 v[130:133], v[158:161], v[166:169], v[130:133]
	v_mfma_f32_16x16x32_bf16 v[126:129], v[150:153], v[174:177], v[126:129]
	v_mfma_f32_16x16x32_bf16 v[122:125], v[158:161], v[174:177], v[122:125]
	v_mfma_f32_16x16x32_bf16 v[118:121], v[150:153], v[182:185], v[118:121]
	v_mfma_f32_16x16x32_bf16 v[114:117], v[158:161], v[182:185], v[114:117]
	v_mfma_f32_16x16x32_bf16 v[110:113], v[150:153], v[190:193], v[110:113]
	v_mfma_f32_16x16x32_bf16 v[106:109], v[158:161], v[190:193], v[106:109]
	v_mfma_f32_16x16x32_bf16 v[74:77], v[154:157], v[170:173], v[74:77]
	v_mfma_f32_16x16x32_bf16 v[130:133], v[162:165], v[170:173], v[130:133]
	v_mfma_f32_16x16x32_bf16 v[126:129], v[154:157], v[178:181], v[126:129]
	v_mfma_f32_16x16x32_bf16 v[122:125], v[162:165], v[178:181], v[122:125]
	v_mfma_f32_16x16x32_bf16 v[118:121], v[154:157], v[186:189], v[118:121]
	v_mfma_f32_16x16x32_bf16 v[114:117], v[162:165], v[186:189], v[114:117]
	v_mfma_f32_16x16x32_bf16 v[110:113], v[154:157], v[194:197], v[110:113]
	v_mfma_f32_16x16x32_bf16 v[106:109], v[162:165], v[194:197], v[106:109]
	v_mfma_f32_16x16x32_bf16 v[102:105], v[134:137], v[166:169], v[102:105]
	v_mfma_f32_16x16x32_bf16 v[98:101], v[142:145], v[166:169], v[98:101]
	v_mfma_f32_16x16x32_bf16 v[94:97], v[134:137], v[174:177], v[94:97]
	v_mfma_f32_16x16x32_bf16 v[90:93], v[142:145], v[174:177], v[90:93]
	v_mfma_f32_16x16x32_bf16 v[86:89], v[134:137], v[182:185], v[86:89]
	v_mfma_f32_16x16x32_bf16 v[82:85], v[142:145], v[182:185], v[82:85]
	v_mfma_f32_16x16x32_bf16 v[78:81], v[134:137], v[190:193], v[78:81]
	v_mfma_f32_16x16x32_bf16 v[70:73], v[142:145], v[190:193], v[70:73]
	v_mfma_f32_16x16x32_bf16 v[102:105], v[138:141], v[170:173], v[102:105]
	v_mfma_f32_16x16x32_bf16 v[98:101], v[146:149], v[170:173], v[98:101]
	v_mfma_f32_16x16x32_bf16 v[94:97], v[138:141], v[178:181], v[94:97]
	v_mfma_f32_16x16x32_bf16 v[90:93], v[146:149], v[178:181], v[90:93]
	v_mfma_f32_16x16x32_bf16 v[86:89], v[138:141], v[186:189], v[86:89]
	v_mfma_f32_16x16x32_bf16 v[82:85], v[146:149], v[186:189], v[82:85]
	v_mfma_f32_16x16x32_bf16 v[78:81], v[138:141], v[194:197], v[78:81]
	v_mfma_f32_16x16x32_bf16 v[70:73], v[146:149], v[194:197], v[70:73]
	s_setprio 0
	s_barrier
	s_add_i32 s8, s59, s13
	v_lshl_add_u64 v[218:219], s[38:39], 0, v[204:205]
	s_mov_b32 m0, s8
	ds_read_b128 v[190:193], v213 offset:16384
	ds_read_b128 v[194:197], v213 offset:17408
	ds_read_b128 v[182:185], v213 offset:18432
	ds_read_b128 v[186:189], v213 offset:19456
	ds_read_b128 v[174:177], v213 offset:20480
	ds_read_b128 v[178:181], v213 offset:21504
	ds_read_b128 v[166:169], v213 offset:22528
	ds_read_b128 v[170:173], v213 offset:23552
	global_load_lds_dwordx4 v[218:219], off
	s_add_i32 m0, s8, 0x2000
	s_add_u32 s8, s38, 0x40000
	v_lshl_add_u64 v[220:221], s[38:39], 0, v[206:207]
	s_addc_u32 s9, s39, 0
	s_add_i32 s33, s33, s13
	global_load_lds_dwordx4 v[220:221], off
	v_lshl_add_u64 v[230:231], s[8:9], 0, v[204:205]
	s_mov_b32 m0, s33
	v_cndmask_b32_e64 v211, 0, 1, s[4:5]
	global_load_lds_dwordx4 v[230:231], off
	v_lshl_add_u64 v[230:231], s[8:9], 0, v[206:207]
	s_add_i32 m0, s33, 0x2000
	v_cmp_ne_u32_e64 s[8:9], 1, v211
	global_load_lds_dwordx4 v[230:231], off
	s_mov_b32 m0, s15
	s_andn2_b64 vcc, exec, s[4:5]
	global_load_lds_dwordx4 v34, s[40:41]
	s_mov_b32 m0, s17
	s_nop 0
	global_load_lds_dwordx4 v222, s[40:41]
	s_waitcnt vmcnt(8)
	s_waitcnt lgkmcnt(0)
	s_barrier
	s_cbranch_vccnz .LBB0_1037
; #define PG8_STAGE(bufoff, gbase, voff) do { _Pragma("unroll") for (int _i = 0; _i < 2; ++_i) \
;         __builtin_amdgcn_global_load_lds((const unsigned*)((const char*)(gbase) + (voff)[_i]), (LAS unsigned*)(lds + (bufoff) + ldsw + _i * 8192), 16, 0, 0); } while (0)
; #define PG8_LDA(dst, b, h) do { _Pragma("unroll") for (int m = 0; m < 4; ++m) _Pragma("unroll") for (int k = 0; k < 2; ++k) dst[m][k] = *(const LAS bf16x8*)(lds + PG8_SA(b, h) + aoff + m * 2048 + k * 1024); } while (0)
; #define PG8_LDB(dst, b, h) do { _Pragma("unroll") for (int n = 0; n < 2; ++n) _Pragma("unroll") for (int k = 0; k < 2; ++k) dst[n][k] = *(const LAS bf16x8*)(lds + PG8_SB(b, h) + boff + n * 2048 + k * 1024); } while (0)
; #define PG8_MMA(ai, bj, At, Bt) do { __builtin_amdgcn_s_setprio(1); _Pragma("unroll") for (int m = 0; m < 4; ++m) _Pragma("unroll") for (int n = 0; n < 2; ++n) _Pragma("unroll") for (int k = 0; k < 2; ++k) \
;         acc[ai][bj][m][n] = __builtin_amdgcn_mfma_f32_16x16x32_bf16(Bt[n][k], At[m][k], acc[ai][bj][m][n], 0, 0, 0); __builtin_amdgcn_s_setprio(0); } while (0)
; #define PG8_WAIT_V(n) asm volatile("s_waitcnt vmcnt(" #n ")" ::: "memory")
; #define PG8_WAIT_L(n) asm volatile("s_waitcnt lgkmcnt(" #n ")" ::: "memory")
; #define PG8_BAR __builtin_amdgcn_s_barrier()
; #define PG8_SCHED __builtin_amdgcn_sched_barrier(0)
; #define PG8_STAGE(bufoff, gbase, voff) do { _Pragma("unroll") for (int _i = 0; _i < 2; ++_i) \
;         __builtin_amdgcn_global_load_lds((const unsigned*)((const char*)(gbase) + (voff)[_i]), (LAS unsigned*)(lds + (bufoff) + ldsw + _i * 8192), 16, 0, 0); } while (0)
; #define PG8_WAIT_V(n) asm volatile("s_waitcnt vmcnt(" #n ")" ::: "memory")
; #define PG8_WAIT_L(n) asm volatile("s_waitcnt lgkmcnt(" #n ")" ::: "memory")
; #define PG8_BAR __builtin_amdgcn_s_barrier()
; template <class Epi, class Sched>
; __device__ __forceinline__ void gemm_phase_gather(LAS unsigned char* lds, const int K, const Sched& S, const Epi& E, const char* Ag, const int* list, const LAS int* seg) {
;     ...
;             PG8_WAIT_V(8); PG8_WAIT_L(0); PG8_BAR; if (hi_on) { PG8_MMA(1, 0, At, B0); PG8_MMA(1, 1, At, B1); } PG8_BAR; PG8_SCHED;
;             PG8_LDB(B0, 1, 0); PG8_LDB(B1, 1, 1); PG8_SCHED; PG8_LDA(At, 1, 0); PG8_STAGE(PG8_SA(0, 1), a2, x1);
;             PG8_WAIT_V(8); PG8_WAIT_L(0); PG8_BAR; PG8_MMA(0, 0, At, B0); PG8_MMA(0, 1, At, B1); PG8_BAR; PG8_SCHED;
	s_setprio 1
	s_waitcnt lgkmcnt(0)
	v_mfma_f32_16x16x32_bf16 v[66:69], v[150:153], v[190:193], v[66:69]
	v_mfma_f32_16x16x32_bf16 v[62:65], v[158:161], v[190:193], v[62:65]
	v_mfma_f32_16x16x32_bf16 v[58:61], v[150:153], v[182:185], v[58:61]
	v_mfma_f32_16x16x32_bf16 v[54:57], v[158:161], v[182:185], v[54:57]
	v_mfma_f32_16x16x32_bf16 v[50:53], v[150:153], v[174:177], v[50:53]
	v_mfma_f32_16x16x32_bf16 v[46:49], v[158:161], v[174:177], v[46:49]
	v_mfma_f32_16x16x32_bf16 v[42:45], v[150:153], v[166:169], v[42:45]
	v_mfma_f32_16x16x32_bf16 v[38:41], v[158:161], v[166:169], v[38:41]
	v_mfma_f32_16x16x32_bf16 v[66:69], v[154:157], v[194:197], v[66:69]
	v_mfma_f32_16x16x32_bf16 v[62:65], v[162:165], v[194:197], v[62:65]
	v_mfma_f32_16x16x32_bf16 v[58:61], v[154:157], v[186:189], v[58:61]
	v_mfma_f32_16x16x32_bf16 v[54:57], v[162:165], v[186:189], v[54:57]
	v_mfma_f32_16x16x32_bf16 v[50:53], v[154:157], v[178:181], v[50:53]
	v_mfma_f32_16x16x32_bf16 v[46:49], v[162:165], v[178:181], v[46:49]
	v_mfma_f32_16x16x32_bf16 v[42:45], v[154:157], v[170:173], v[42:45]
	v_mfma_f32_16x16x32_bf16 v[38:41], v[162:165], v[170:173], v[38:41]
	v_mfma_f32_16x16x32_bf16 v[30:33], v[134:137], v[190:193], v[30:33]
	v_mfma_f32_16x16x32_bf16 v[26:29], v[142:145], v[190:193], v[26:29]
	v_mfma_f32_16x16x32_bf16 v[22:25], v[134:137], v[182:185], v[22:25]
	v_mfma_f32_16x16x32_bf16 v[18:21], v[142:145], v[182:185], v[18:21]
	v_mfma_f32_16x16x32_bf16 v[14:17], v[134:137], v[174:177], v[14:17]
	v_mfma_f32_16x16x32_bf16 v[10:13], v[142:145], v[174:177], v[10:13]
	v_mfma_f32_16x16x32_bf16 v[6:9], v[134:137], v[166:169], v[6:9]
	v_mfma_f32_16x16x32_bf16 v[2:5], v[142:145], v[166:169], v[2:5]
	v_mfma_f32_16x16x32_bf16 v[30:33], v[138:141], v[194:197], v[30:33]
	v_mfma_f32_16x16x32_bf16 v[26:29], v[146:149], v[194:197], v[26:29]
	v_mfma_f32_16x16x32_bf16 v[22:25], v[138:141], v[186:189], v[22:25]
	v_mfma_f32_16x16x32_bf16 v[18:21], v[146:149], v[186:189], v[18:21]
	v_mfma_f32_16x16x32_bf16 v[14:17], v[138:141], v[178:181], v[14:17]
	v_mfma_f32_16x16x32_bf16 v[10:13], v[146:149], v[178:181], v[10:13]
	v_mfma_f32_16x16x32_bf16 v[6:9], v[138:141], v[170:173], v[6:9]
	v_mfma_f32_16x16x32_bf16 v[2:5], v[146:149], v[170:173], v[2:5]
	s_setprio 0
.LBB0_1037:
	v_mov_b32_e32 v223, v35
	v_lshl_add_u64 v[230:231], s[40:41], 0, v[34:35]
	v_lshl_add_u64 v[222:223], s[40:41], 0, v[222:223]
	v_cndmask_b32_e64 v34, v210, v229, s[6:7]
	v_cndmask_b32_e64 v211, v214, v249, s[6:7]
	s_barrier
	s_add_i32 s6, 0, 0x18000
	s_add_i32 s33, 0, 0x1c000
	v_add_u32_e32 v134, s6, v248
	v_add_u32_e32 v146, s33, v248
	ds_read_b128 v[150:153], v134
	ds_read_b128 v[154:157], v134 offset:1024
	ds_read_b128 v[158:161], v134 offset:2048
	ds_read_b128 v[162:165], v134 offset:3072
	ds_read_b128 v[134:137], v146
	ds_read_b128 v[138:141], v146 offset:1024
	ds_read_b128 v[142:145], v146 offset:2048
	ds_read_b128 v[146:149], v146 offset:3072
	s_mov_b32 m0, s45
	s_waitcnt lgkmcnt(0)
	ds_read_b128 v[166:169], v213 offset:32768
	ds_read_b128 v[170:173], v213 offset:33792
	ds_read_b128 v[174:177], v213 offset:34816
	ds_read_b128 v[178:181], v213 offset:35840
	ds_read_b128 v[182:185], v213 offset:36864
	ds_read_b128 v[186:189], v213 offset:37888
	ds_read_b128 v[190:193], v213 offset:38912
	ds_read_b128 v[194:197], v213 offset:39936
	global_load_lds_dwordx4 v34, s[40:41]
	s_mov_b32 m0, s46
	s_nop 0
	global_load_lds_dwordx4 v211, s[40:41]
	s_waitcnt vmcnt(8)
	s_waitcnt lgkmcnt(0)
	s_barrier
	s_setprio 1
	s_waitcnt lgkmcnt(0)
	v_mfma_f32_16x16x32_bf16 v[74:77], v[150:153], v[166:169], v[74:77]
	v_mfma_f32_16x16x32_bf16 v[130:133], v[158:161], v[166:169], v[130:133]
	v_mfma_f32_16x16x32_bf16 v[126:129], v[150:153], v[174:177], v[126:129]
	v_mfma_f32_16x16x32_bf16 v[122:125], v[158:161], v[174:177], v[122:125]
	v_mfma_f32_16x16x32_bf16 v[118:121], v[150:153], v[182:185], v[118:121]
	v_mfma_f32_16x16x32_bf16 v[114:117], v[158:161], v[182:185], v[114:117]
	v_mfma_f32_16x16x32_bf16 v[110:113], v[150:153], v[190:193], v[110:113]
	v_mfma_f32_16x16x32_bf16 v[106:109], v[158:161], v[190:193], v[106:109]
	v_mfma_f32_16x16x32_bf16 v[74:77], v[154:157], v[170:173], v[74:77]
	v_mfma_f32_16x16x32_bf16 v[130:133], v[162:165], v[170:173], v[130:133]
	v_mfma_f32_16x16x32_bf16 v[126:129], v[154:157], v[178:181], v[126:129]
	v_mfma_f32_16x16x32_bf16 v[122:125], v[162:165], v[178:181], v[122:125]
	v_mfma_f32_16x16x32_bf16 v[118:121], v[154:157], v[186:189], v[118:121]
	v_mfma_f32_16x16x32_bf16 v[114:117], v[162:165], v[186:189], v[114:117]
	v_mfma_f32_16x16x32_bf16 v[110:113], v[154:157], v[194:197], v[110:113]
	v_mfma_f32_16x16x32_bf16 v[106:109], v[162:165], v[194:197], v[106:109]
	v_mfma_f32_16x16x32_bf16 v[102:105], v[134:137], v[166:169], v[102:105]
	v_mfma_f32_16x16x32_bf16 v[98:101], v[142:145], v[166:169], v[98:101]
	v_mfma_f32_16x16x32_bf16 v[94:97], v[134:137], v[174:177], v[94:97]
	v_mfma_f32_16x16x32_bf16 v[90:93], v[142:145], v[174:177], v[90:93]
	v_mfma_f32_16x16x32_bf16 v[86:89], v[134:137], v[182:185], v[86:89]
	v_mfma_f32_16x16x32_bf16 v[82:85], v[142:145], v[182:185], v[82:85]
	v_mfma_f32_16x16x32_bf16 v[78:81], v[134:137], v[190:193], v[78:81]
	v_mfma_f32_16x16x32_bf16 v[70:73], v[142:145], v[190:193], v[70:73]
	v_mfma_f32_16x16x32_bf16 v[102:105], v[138:141], v[170:173], v[102:105]
	v_mfma_f32_16x16x32_bf16 v[98:101], v[146:149], v[170:173], v[98:101]
	v_mfma_f32_16x16x32_bf16 v[94:97], v[138:141], v[178:181], v[94:97]
	v_mfma_f32_16x16x32_bf16 v[90:93], v[146:149], v[178:181], v[90:93]
	v_mfma_f32_16x16x32_bf16 v[86:89], v[138:141], v[186:189], v[86:89]
	v_mfma_f32_16x16x32_bf16 v[82:85], v[146:149], v[186:189], v[82:85]
	v_mfma_f32_16x16x32_bf16 v[78:81], v[138:141], v[194:197], v[78:81]
	v_mfma_f32_16x16x32_bf16 v[70:73], v[146:149], v[194:197], v[70:73]
	s_setprio 0
	s_barrier
; #define PG8_STAGE(bufoff, gbase, voff) do { _Pragma("unroll") for (int _i = 0; _i < 2; ++_i) \
;         __builtin_amdgcn_global_load_lds((const unsigned*)((const char*)(gbase) + (voff)[_i]), (LAS unsigned*)(lds + (bufoff) + ldsw + _i * 8192), 16, 0, 0); } while (0)
; #define PG8_LDA(dst, b, h) do { _Pragma("unroll") for (int m = 0; m < 4; ++m) _Pragma("unroll") for (int k = 0; k < 2; ++k) dst[m][k] = *(const LAS bf16x8*)(lds + PG8_SA(b, h) + aoff + m * 2048 + k * 1024); } while (0)
; #define PG8_MMA(ai, bj, At, Bt) do { __builtin_amdgcn_s_setprio(1); _Pragma("unroll") for (int m = 0; m < 4; ++m) _Pragma("unroll") for (int n = 0; n < 2; ++n) _Pragma("unroll") for (int k = 0; k < 2; ++k) \
;         acc[ai][bj][m][n] = __builtin_amdgcn_mfma_f32_16x16x32_bf16(Bt[n][k], At[m][k], acc[ai][bj][m][n], 0, 0, 0); __builtin_amdgcn_s_setprio(0); } while (0)
; #define PG8_WAIT_V(n) asm volatile("s_waitcnt vmcnt(" #n ")" ::: "memory")
; #define PG8_WAIT_L(n) asm volatile("s_waitcnt lgkmcnt(" #n ")" ::: "memory")
; #define PG8_BAR __builtin_amdgcn_s_barrier()
; #define PG8_SCHED __builtin_amdgcn_sched_barrier(0)
; #define PG8_STAGE(bufoff, gbase, voff) do { _Pragma("unroll") for (int _i = 0; _i < 2; ++_i) \
;         __builtin_amdgcn_global_load_lds((const unsigned*)((const char*)(gbase) + (voff)[_i]), (LAS unsigned*)(lds + (bufoff) + ldsw + _i * 8192), 16, 0, 0); } while (0)
; #define PG8_LDA(dst, b, h) do { _Pragma("unroll") for (int m = 0; m < 4; ++m) _Pragma("unroll") for (int k = 0; k < 2; ++k) dst[m][k] = *(const LAS bf16x8*)(lds + PG8_SA(b, h) + aoff + m * 2048 + k * 1024); } while (0)
; #define PG8_WAIT_V(n) asm volatile("s_waitcnt vmcnt(" #n ")" ::: "memory")
; #define PG8_WAIT_L(n) asm volatile("s_waitcnt lgkmcnt(" #n ")" ::: "memory")
; #define PG8_BAR __builtin_amdgcn_s_barrier()
; #define PG8_SCHED __builtin_amdgcn_sched_barrier(0)
; template <class Epi, class Sched>
; __device__ __forceinline__ void gemm_phase_gather(LAS unsigned char* lds, const int K, const Sched& S, const Epi& E, const char* Ag, const int* list, const LAS int* seg) {
;     ...
;             PG8_LDA(At, 1, 1); PG8_STAGE(PG8_SB(1, 0), b3, voffB); PG8_STAGE(PG8_SB(1, 1), b3 + hstep, voffB); PG8_STAGE(PG8_SA(1, 0), a3, x0);
;             PG8_WAIT_V(8); PG8_WAIT_L(0); PG8_BAR; if (hi_on) { PG8_MMA(1, 0, At, B0); PG8_MMA(1, 1, At, B1); } PG8_BAR; PG8_SCHED;
;         }
	s_add_i32 s6, s6, s13
	v_lshl_add_u64 v[218:219], v[218:219], 0, s[88:89]
	s_mov_b32 m0, s6
	ds_read_b128 v[190:193], v213 offset:49152
	ds_read_b128 v[194:197], v213 offset:50176
	ds_read_b128 v[182:185], v213 offset:51200
	ds_read_b128 v[186:189], v213 offset:52224
	ds_read_b128 v[174:177], v213 offset:53248
	ds_read_b128 v[178:181], v213 offset:54272
	ds_read_b128 v[166:169], v213 offset:55296
	ds_read_b128 v[170:173], v213 offset:56320
	global_load_lds_dwordx4 v[218:219], off
	s_add_i32 m0, s6, 0x2000
	s_add_u32 s6, s38, 0x40080
	v_lshl_add_u64 v[218:219], v[220:221], 0, s[88:89]
	s_addc_u32 s7, s39, 0
	s_add_i32 s33, s33, s13
	global_load_lds_dwordx4 v[218:219], off
	v_lshl_add_u64 v[218:219], s[6:7], 0, v[204:205]
	s_mov_b32 m0, s33
	s_and_b64 vcc, exec, s[8:9]
	global_load_lds_dwordx4 v[218:219], off
	v_lshl_add_u64 v[218:219], s[6:7], 0, v[206:207]
	s_add_i32 m0, s33, 0x2000
	s_nop 0
	global_load_lds_dwordx4 v[218:219], off
	v_lshl_add_u64 v[218:219], v[230:231], 0, s[88:89]
	s_mov_b32 m0, s47
	s_nop 0
	global_load_lds_dwordx4 v[218:219], off
	v_lshl_add_u64 v[218:219], v[222:223], 0, s[88:89]
	s_mov_b32 m0, s48
	s_nop 0
	global_load_lds_dwordx4 v[218:219], off
	s_waitcnt vmcnt(8)
	s_waitcnt lgkmcnt(0)
	s_barrier
	s_cbranch_vccnz .LBB0_1034
	s_setprio 1
	s_waitcnt lgkmcnt(0)
	v_mfma_f32_16x16x32_bf16 v[66:69], v[150:153], v[190:193], v[66:69]
	v_mfma_f32_16x16x32_bf16 v[62:65], v[158:161], v[190:193], v[62:65]
	v_mfma_f32_16x16x32_bf16 v[58:61], v[150:153], v[182:185], v[58:61]
	v_mfma_f32_16x16x32_bf16 v[54:57], v[158:161], v[182:185], v[54:57]
	v_mfma_f32_16x16x32_bf16 v[50:53], v[150:153], v[174:177], v[50:53]
	v_mfma_f32_16x16x32_bf16 v[46:49], v[158:161], v[174:177], v[46:49]
	v_mfma_f32_16x16x32_bf16 v[42:45], v[150:153], v[166:169], v[42:45]
	v_mfma_f32_16x16x32_bf16 v[38:41], v[158:161], v[166:169], v[38:41]
	v_mfma_f32_16x16x32_bf16 v[66:69], v[154:157], v[194:197], v[66:69]
	v_mfma_f32_16x16x32_bf16 v[62:65], v[162:165], v[194:197], v[62:65]
	v_mfma_f32_16x16x32_bf16 v[58:61], v[154:157], v[186:189], v[58:61]
	v_mfma_f32_16x16x32_bf16 v[54:57], v[162:165], v[186:189], v[54:57]
	v_mfma_f32_16x16x32_bf16 v[50:53], v[154:157], v[178:181], v[50:53]
	v_mfma_f32_16x16x32_bf16 v[46:49], v[162:165], v[178:181], v[46:49]
	v_mfma_f32_16x16x32_bf16 v[42:45], v[154:157], v[170:173], v[42:45]
	v_mfma_f32_16x16x32_bf16 v[38:41], v[162:165], v[170:173], v[38:41]
	v_mfma_f32_16x16x32_bf16 v[30:33], v[134:137], v[190:193], v[30:33]
	v_mfma_f32_16x16x32_bf16 v[26:29], v[142:145], v[190:193], v[26:29]
	v_mfma_f32_16x16x32_bf16 v[22:25], v[134:137], v[182:185], v[22:25]
	v_mfma_f32_16x16x32_bf16 v[18:21], v[142:145], v[182:185], v[18:21]
	v_mfma_f32_16x16x32_bf16 v[14:17], v[134:137], v[174:177], v[14:17]
	v_mfma_f32_16x16x32_bf16 v[10:13], v[142:145], v[174:177], v[10:13]
	v_mfma_f32_16x16x32_bf16 v[6:9], v[134:137], v[166:169], v[6:9]
	v_mfma_f32_16x16x32_bf16 v[2:5], v[142:145], v[166:169], v[2:5]
	v_mfma_f32_16x16x32_bf16 v[30:33], v[138:141], v[194:197], v[30:33]
	v_mfma_f32_16x16x32_bf16 v[26:29], v[146:149], v[194:197], v[26:29]
	v_mfma_f32_16x16x32_bf16 v[22:25], v[138:141], v[186:189], v[22:25]
	v_mfma_f32_16x16x32_bf16 v[18:21], v[146:149], v[186:189], v[18:21]
	v_mfma_f32_16x16x32_bf16 v[14:17], v[138:141], v[178:181], v[14:17]
	v_mfma_f32_16x16x32_bf16 v[10:13], v[146:149], v[178:181], v[10:13]
	v_mfma_f32_16x16x32_bf16 v[6:9], v[138:141], v[170:173], v[6:9]
	v_mfma_f32_16x16x32_bf16 v[2:5], v[146:149], v[170:173], v[2:5]
	s_setprio 0
	s_branch .LBB0_1034

; #define PG8_STAGE(bufoff, gbase, voff) do { _Pragma("unroll") for (int _i = 0; _i < 2; ++_i) \
;         __builtin_amdgcn_global_load_lds((const unsigned*)((const char*)(gbase) + (voff)[_i]), (LAS unsigned*)(lds + (bufoff) + ldsw + _i * 8192), 16, 0, 0); } while (0)
; #define PG8_LDA(dst, b, h) do { _Pragma("unroll") for (int m = 0; m < 4; ++m) _Pragma("unroll") for (int k = 0; k < 2; ++k) dst[m][k] = *(const LAS bf16x8*)(lds + PG8_SA(b, h) + aoff + m * 2048 + k * 1024); } while (0)
; #define PG8_LDB(dst, b, h) do { _Pragma("unroll") for (int n = 0; n < 2; ++n) _Pragma("unroll") for (int k = 0; k < 2; ++k) dst[n][k] = *(const LAS bf16x8*)(lds + PG8_SB(b, h) + boff + n * 2048 + k * 1024); } while (0)
; #define PG8_MMA(ai, bj, At, Bt) do { __builtin_amdgcn_s_setprio(1); _Pragma("unroll") for (int m = 0; m < 4; ++m) _Pragma("unroll") for (int n = 0; n < 2; ++n) _Pragma("unroll") for (int k = 0; k < 2; ++k) \
;         acc[ai][bj][m][n] = __builtin_amdgcn_mfma_f32_16x16x32_bf16(Bt[n][k], At[m][k], acc[ai][bj][m][n], 0, 0, 0); __builtin_amdgcn_s_setprio(0); } while (0)
; #define PG8_WAIT_V(n) asm volatile("s_waitcnt vmcnt(" #n ")" ::: "memory")
; #define PG8_WAIT_L(n) asm volatile("s_waitcnt lgkmcnt(" #n ")" ::: "memory")
; #define PG8_BAR __builtin_amdgcn_s_barrier()
; #define PG8_SCHED __builtin_amdgcn_sched_barrier(0)
; #define PG8_WAIT_V(n) asm volatile("s_waitcnt vmcnt(" #n ")" ::: "memory")
; #define PG8_WAIT_L(n) asm volatile("s_waitcnt lgkmcnt(" #n ")" ::: "memory")
;     ...
;         for (int t = 0; t < nt; t += 2) {
;             const bool last = (t == nt - 2);
;             const char* a1 = cA + (size_t)(t + 1) * kstepA;
;             const char* a2 = last ? nA : cA + (size_t)(t + 2) * kstepA; const char* b2 = last ? nB : cB + (size_t)(t + 2) * kstep;
;             const char* a3 = a2 + kstepA; const char* b3 = b2 + kstep;
;             PG8_LDB(B0, 0, 0); PG8_LDB(B1, 0, 1); PG8_SCHED; PG8_LDA(At, 0, 0); PG8_STAGE(PG8_SA(1, 1), a1 + hstepA, voffA);
;             PG8_WAIT_V(8); PG8_WAIT_L(0); PG8_BAR; PG8_MMA(0, 0, At, B0); PG8_MMA(0, 1, At, B1); PG8_BAR; PG8_SCHED;
;             PG8_LDA(At, 0, 1); PG8_STAGE(PG8_SB(0, 0), b2, voffB); PG8_STAGE(PG8_SB(0, 1), b2 + hstep, voffB); PG8_STAGE(PG8_SA(0, 0), a2, voffA);
;             PG8_WAIT_V(8); PG8_WAIT_L(0); PG8_BAR; if (hi_on) { PG8_MMA(1, 0, At, B0); PG8_MMA(1, 1, At, B1); } PG8_BAR; PG8_SCHED;
.LBB0_1294:
	s_add_u32 s8, s14, s34
	s_addc_u32 s9, s15, s35
	s_add_u32 s8, s8, 0x100
	s_addc_u32 s9, s9, 0
	s_add_u32 s33, s55, s34
	s_addc_u32 s36, s66, s35
	s_add_i32 s58, 0, 0x10000
	s_cmpk_eq_i32 s34, 0x300
	s_cselect_b32 s39, s29, s9
	s_cselect_b32 s38, s28, s8
	v_add_u32_e32 v34, s58, v227
	s_cselect_b32 s37, s27, s36
	s_cselect_b32 s36, s26, s33
	s_add_i32 s33, 0, 0x14000
	ds_read_b128 v[150:153], v34
	ds_read_b128 v[154:157], v34 offset:1024
	ds_read_b128 v[158:161], v34 offset:2048
	ds_read_b128 v[162:165], v34 offset:3072
	v_add_u32_e32 v34, s33, v227
	ds_read_b128 v[134:137], v34
	ds_read_b128 v[138:141], v34 offset:1024
	ds_read_b128 v[142:145], v34 offset:2048
	ds_read_b128 v[146:149], v34 offset:3072
	v_lshl_add_u64 v[218:219], v[36:37], 0, s[34:35]
	s_add_i32 m0, s13, 0xc000
	s_waitcnt lgkmcnt(0)
	ds_read_b128 v[166:169], v245
	ds_read_b128 v[170:173], v245 offset:1024
	ds_read_b128 v[174:177], v245 offset:2048
	ds_read_b128 v[178:181], v245 offset:3072
	ds_read_b128 v[182:185], v245 offset:4096
	ds_read_b128 v[186:189], v245 offset:5120
	ds_read_b128 v[190:193], v245 offset:6144
	ds_read_b128 v[194:197], v245 offset:7168
	global_load_lds_dwordx4 v[218:219], off
	v_lshl_add_u64 v[218:219], v[216:217], 0, s[34:35]
	s_add_i32 m0, s13, 0xe000
	s_nop 0
	global_load_lds_dwordx4 v[218:219], off
	s_waitcnt vmcnt(8)
	s_waitcnt lgkmcnt(0)
	s_barrier
	s_setprio 1
	s_waitcnt lgkmcnt(0)
	v_mfma_f32_16x16x32_bf16 v[130:133], v[150:153], v[166:169], v[130:133]
	v_mfma_f32_16x16x32_bf16 v[126:129], v[158:161], v[166:169], v[126:129]
	v_mfma_f32_16x16x32_bf16 v[122:125], v[150:153], v[174:177], v[122:125]
	v_mfma_f32_16x16x32_bf16 v[118:121], v[158:161], v[174:177], v[118:121]
	v_mfma_f32_16x16x32_bf16 v[114:117], v[150:153], v[182:185], v[114:117]
	v_mfma_f32_16x16x32_bf16 v[110:113], v[158:161], v[182:185], v[110:113]
	v_mfma_f32_16x16x32_bf16 v[106:109], v[150:153], v[190:193], v[106:109]
	v_mfma_f32_16x16x32_bf16 v[102:105], v[158:161], v[190:193], v[102:105]
	v_mfma_f32_16x16x32_bf16 v[130:133], v[154:157], v[170:173], v[130:133]
	v_mfma_f32_16x16x32_bf16 v[126:129], v[162:165], v[170:173], v[126:129]
	v_mfma_f32_16x16x32_bf16 v[122:125], v[154:157], v[178:181], v[122:125]
	v_mfma_f32_16x16x32_bf16 v[118:121], v[162:165], v[178:181], v[118:121]
	v_mfma_f32_16x16x32_bf16 v[114:117], v[154:157], v[186:189], v[114:117]
	v_mfma_f32_16x16x32_bf16 v[110:113], v[162:165], v[186:189], v[110:113]
	v_mfma_f32_16x16x32_bf16 v[106:109], v[154:157], v[194:197], v[106:109]
	v_mfma_f32_16x16x32_bf16 v[102:105], v[162:165], v[194:197], v[102:105]
	v_mfma_f32_16x16x32_bf16 v[98:101], v[134:137], v[166:169], v[98:101]
	v_mfma_f32_16x16x32_bf16 v[94:97], v[142:145], v[166:169], v[94:97]
	v_mfma_f32_16x16x32_bf16 v[90:93], v[134:137], v[174:177], v[90:93]
	v_mfma_f32_16x16x32_bf16 v[86:89], v[142:145], v[174:177], v[86:89]
	v_mfma_f32_16x16x32_bf16 v[82:85], v[134:137], v[182:185], v[82:85]
	v_mfma_f32_16x16x32_bf16 v[78:81], v[142:145], v[182:185], v[78:81]
	v_mfma_f32_16x16x32_bf16 v[74:77], v[134:137], v[190:193], v[74:77]
	v_mfma_f32_16x16x32_bf16 v[70:73], v[142:145], v[190:193], v[70:73]
	v_mfma_f32_16x16x32_bf16 v[98:101], v[138:141], v[170:173], v[98:101]
	v_mfma_f32_16x16x32_bf16 v[94:97], v[146:149], v[170:173], v[94:97]
	v_mfma_f32_16x16x32_bf16 v[90:93], v[138:141], v[178:181], v[90:93]
	v_mfma_f32_16x16x32_bf16 v[86:89], v[146:149], v[178:181], v[86:89]
	v_mfma_f32_16x16x32_bf16 v[82:85], v[138:141], v[186:189], v[82:85]
	v_mfma_f32_16x16x32_bf16 v[78:81], v[146:149], v[186:189], v[78:81]
	v_mfma_f32_16x16x32_bf16 v[74:77], v[138:141], v[194:197], v[74:77]
	v_mfma_f32_16x16x32_bf16 v[70:73], v[146:149], v[194:197], v[70:73]
	s_setprio 0
	s_barrier
	s_add_i32 s8, s58, s11
	v_lshl_add_u64 v[218:219], s[36:37], 0, v[206:207]
	s_mov_b32 m0, s8
	ds_read_b128 v[190:193], v245 offset:16384
	ds_read_b128 v[194:197], v245 offset:17408
	ds_read_b128 v[182:185], v245 offset:18432
	ds_read_b128 v[186:189], v245 offset:19456
	ds_read_b128 v[174:177], v245 offset:20480
	ds_read_b128 v[178:181], v245 offset:21504
	ds_read_b128 v[166:169], v245 offset:22528
	ds_read_b128 v[170:173], v245 offset:23552
	global_load_lds_dwordx4 v[218:219], off
	s_add_i32 m0, s8, 0x2000
	s_add_u32 s8, s36, 0x20000
	v_lshl_add_u64 v[220:221], s[36:37], 0, v[210:211]
	s_addc_u32 s9, s37, 0
	s_add_i32 s33, s33, s11
	global_load_lds_dwordx4 v[220:221], off
	v_lshl_add_u64 v[222:223], s[8:9], 0, v[206:207]
	s_mov_b32 m0, s33
	v_lshl_add_u64 v[224:225], s[38:39], 0, v[208:209]
	global_load_lds_dwordx4 v[222:223], off
	v_lshl_add_u64 v[222:223], s[8:9], 0, v[210:211]
	s_add_i32 m0, s33, 0x2000
	v_cndmask_b32_e64 v34, 0, 1, s[6:7]
	global_load_lds_dwordx4 v[222:223], off
	v_lshl_add_u64 v[222:223], s[38:39], 0, v[204:205]
	s_mov_b32 m0, s13
	v_cmp_ne_u32_e64 s[8:9], 1, v34
	global_load_lds_dwordx4 v[222:223], off
	s_mov_b32 m0, s43
	s_andn2_b64 vcc, exec, s[6:7]
	global_load_lds_dwordx4 v[224:225], off
	s_waitcnt vmcnt(8)
	s_waitcnt lgkmcnt(0)
	s_barrier
	s_cbranch_vccnz .LBB0_1296
; #define PG8_MMA(ai, bj, At, Bt) do { __builtin_amdgcn_s_setprio(1); _Pragma("unroll") for (int m = 0; m < 4; ++m) _Pragma("unroll") for (int n = 0; n < 2; ++n) _Pragma("unroll") for (int k = 0; k < 2; ++k) \
;         acc[ai][bj][m][n] = __builtin_amdgcn_mfma_f32_16x16x32_bf16(Bt[n][k], At[m][k], acc[ai][bj][m][n], 0, 0, 0); __builtin_amdgcn_s_setprio(0); } while (0)
; #define PG8_WAIT_V(n) asm volatile("s_waitcnt vmcnt(" #n ")" ::: "memory")
; #define PG8_WAIT_L(n) asm volatile("s_waitcnt lgkmcnt(" #n ")" ::: "memory")
; #define PG8_BAR __builtin_amdgcn_s_barrier()
; #define PG8_SCHED __builtin_amdgcn_sched_barrier(0)
; #define PG8_MMA(ai, bj, At, Bt) do { __builtin_amdgcn_s_setprio(1); _Pragma("unroll") for (int m = 0; m < 4; ++m) _Pragma("unroll") for (int n = 0; n < 2; ++n) _Pragma("unroll") for (int k = 0; k < 2; ++k) \
;         acc[ai][bj][m][n] = __builtin_amdgcn_mfma_f32_16x16x32_bf16(Bt[n][k], At[m][k], acc[ai][bj][m][n], 0, 0, 0); __builtin_amdgcn_s_setprio(0); } while (0)
; #define PG8_WAIT_V(n) asm volatile("s_waitcnt vmcnt(" #n ")" ::: "memory")
; #define PG8_WAIT_L(n) asm volatile("s_waitcnt lgkmcnt(" #n ")" ::: "memory")
; #define PG8_BAR __builtin_amdgcn_s_barrier()
; #define PG8_SCHED __builtin_amdgcn_sched_barrier(0)
;     ...
;             PG8_WAIT_V(8); PG8_WAIT_L(0); PG8_BAR; if (hi_on) { PG8_MMA(1, 0, At, B0); PG8_MMA(1, 1, At, B1); } PG8_BAR; PG8_SCHED;
	s_setprio 1
	s_waitcnt lgkmcnt(0)
	v_mfma_f32_16x16x32_bf16 v[66:69], v[150:153], v[190:193], v[66:69]
	v_mfma_f32_16x16x32_bf16 v[62:65], v[158:161], v[190:193], v[62:65]
	v_mfma_f32_16x16x32_bf16 v[58:61], v[150:153], v[182:185], v[58:61]
	v_mfma_f32_16x16x32_bf16 v[54:57], v[158:161], v[182:185], v[54:57]
	v_mfma_f32_16x16x32_bf16 v[50:53], v[150:153], v[174:177], v[50:53]
	v_mfma_f32_16x16x32_bf16 v[46:49], v[158:161], v[174:177], v[46:49]
	v_mfma_f32_16x16x32_bf16 v[42:45], v[150:153], v[166:169], v[42:45]
	v_mfma_f32_16x16x32_bf16 v[38:41], v[158:161], v[166:169], v[38:41]
	v_mfma_f32_16x16x32_bf16 v[66:69], v[154:157], v[194:197], v[66:69]
	v_mfma_f32_16x16x32_bf16 v[62:65], v[162:165], v[194:197], v[62:65]
	v_mfma_f32_16x16x32_bf16 v[58:61], v[154:157], v[186:189], v[58:61]
	v_mfma_f32_16x16x32_bf16 v[54:57], v[162:165], v[186:189], v[54:57]
	v_mfma_f32_16x16x32_bf16 v[50:53], v[154:157], v[178:181], v[50:53]
	v_mfma_f32_16x16x32_bf16 v[46:49], v[162:165], v[178:181], v[46:49]
	v_mfma_f32_16x16x32_bf16 v[42:45], v[154:157], v[170:173], v[42:45]
	v_mfma_f32_16x16x32_bf16 v[38:41], v[162:165], v[170:173], v[38:41]
	v_mfma_f32_16x16x32_bf16 v[30:33], v[134:137], v[190:193], v[30:33]
	v_mfma_f32_16x16x32_bf16 v[26:29], v[142:145], v[190:193], v[26:29]
	v_mfma_f32_16x16x32_bf16 v[22:25], v[134:137], v[182:185], v[22:25]
	v_mfma_f32_16x16x32_bf16 v[18:21], v[142:145], v[182:185], v[18:21]
	v_mfma_f32_16x16x32_bf16 v[14:17], v[134:137], v[174:177], v[14:17]
	v_mfma_f32_16x16x32_bf16 v[10:13], v[142:145], v[174:177], v[10:13]
	v_mfma_f32_16x16x32_bf16 v[6:9], v[134:137], v[166:169], v[6:9]
	v_mfma_f32_16x16x32_bf16 v[2:5], v[142:145], v[166:169], v[2:5]
	v_mfma_f32_16x16x32_bf16 v[30:33], v[138:141], v[194:197], v[30:33]
	v_mfma_f32_16x16x32_bf16 v[26:29], v[146:149], v[194:197], v[26:29]
	v_mfma_f32_16x16x32_bf16 v[22:25], v[138:141], v[186:189], v[22:25]
	v_mfma_f32_16x16x32_bf16 v[18:21], v[146:149], v[186:189], v[18:21]
	v_mfma_f32_16x16x32_bf16 v[14:17], v[138:141], v[178:181], v[14:17]
	v_mfma_f32_16x16x32_bf16 v[10:13], v[146:149], v[178:181], v[10:13]
	v_mfma_f32_16x16x32_bf16 v[6:9], v[138:141], v[170:173], v[6:9]
	v_mfma_f32_16x16x32_bf16 v[2:5], v[146:149], v[170:173], v[2:5]
	s_setprio 0
; #define PG8_STAGE(bufoff, gbase, voff) do { _Pragma("unroll") for (int _i = 0; _i < 2; ++_i) \
;         __builtin_amdgcn_global_load_lds((const unsigned*)((const char*)(gbase) + (voff)[_i]), (LAS unsigned*)(lds + (bufoff) + ldsw + _i * 8192), 16, 0, 0); } while (0)
; #define PG8_LDA(dst, b, h) do { _Pragma("unroll") for (int m = 0; m < 4; ++m) _Pragma("unroll") for (int k = 0; k < 2; ++k) dst[m][k] = *(const LAS bf16x8*)(lds + PG8_SA(b, h) + aoff + m * 2048 + k * 1024); } while (0)
; #define PG8_LDB(dst, b, h) do { _Pragma("unroll") for (int n = 0; n < 2; ++n) _Pragma("unroll") for (int k = 0; k < 2; ++k) dst[n][k] = *(const LAS bf16x8*)(lds + PG8_SB(b, h) + boff + n * 2048 + k * 1024); } while (0)
; #define PG8_MMA(ai, bj, At, Bt) do { __builtin_amdgcn_s_setprio(1); _Pragma("unroll") for (int m = 0; m < 4; ++m) _Pragma("unroll") for (int n = 0; n < 2; ++n) _Pragma("unroll") for (int k = 0; k < 2; ++k) \
;         acc[ai][bj][m][n] = __builtin_amdgcn_mfma_f32_16x16x32_bf16(Bt[n][k], At[m][k], acc[ai][bj][m][n], 0, 0, 0); __builtin_amdgcn_s_setprio(0); } while (0)
; #define PG8_WAIT_V(n) asm volatile("s_waitcnt vmcnt(" #n ")" ::: "memory")
; #define PG8_WAIT_L(n) asm volatile("s_waitcnt lgkmcnt(" #n ")" ::: "memory")
; #define PG8_BAR __builtin_amdgcn_s_barrier()
; #define PG8_SCHED __builtin_amdgcn_sched_barrier(0)
; #define PG8_STAGE(bufoff, gbase, voff) do { _Pragma("unroll") for (int _i = 0; _i < 2; ++_i) \
;         __builtin_amdgcn_global_load_lds((const unsigned*)((const char*)(gbase) + (voff)[_i]), (LAS unsigned*)(lds + (bufoff) + ldsw + _i * 8192), 16, 0, 0); } while (0)
; #define PG8_LDA(dst, b, h) do { _Pragma("unroll") for (int m = 0; m < 4; ++m) _Pragma("unroll") for (int k = 0; k < 2; ++k) dst[m][k] = *(const LAS bf16x8*)(lds + PG8_SA(b, h) + aoff + m * 2048 + k * 1024); } while (0)
;     ...
;             PG8_LDB(B0, 1, 0); PG8_LDB(B1, 1, 1); PG8_SCHED; PG8_LDA(At, 1, 0); PG8_STAGE(PG8_SA(0, 1), a2 + hstepA, voffA);
;             PG8_WAIT_V(8); PG8_WAIT_L(0); PG8_BAR; PG8_MMA(0, 0, At, B0); PG8_MMA(0, 1, At, B1); PG8_BAR; PG8_SCHED;
;             PG8_LDA(At, 1, 1); PG8_STAGE(PG8_SB(1, 0), b3, voffB); PG8_STAGE(PG8_SB(1, 1), b3 + hstep, voffB); PG8_STAGE(PG8_SA(1, 0), a3, voffA);
;             PG8_WAIT_V(8); PG8_WAIT_L(0); PG8_BAR; if (hi_on) { PG8_MMA(1, 0, At, B0); PG8_MMA(1, 1, At, B1); } PG8_BAR; PG8_SCHED;
;         }
.LBB0_1296:
	s_barrier
	s_add_i32 s33, 0, 0x18000
	v_add_u32_e32 v34, s33, v227
	s_add_i32 s58, 0, 0x1c000
	ds_read_b128 v[150:153], v34
	ds_read_b128 v[154:157], v34 offset:1024
	ds_read_b128 v[158:161], v34 offset:2048
	ds_read_b128 v[162:165], v34 offset:3072
	v_add_u32_e32 v34, s58, v227
	ds_read_b128 v[134:137], v34
	ds_read_b128 v[138:141], v34 offset:1024
	ds_read_b128 v[142:145], v34 offset:2048
	ds_read_b128 v[146:149], v34 offset:3072
	s_add_u32 s38, s38, 0x20000
	s_addc_u32 s39, s39, 0
	s_mov_b32 m0, s44
	v_lshl_add_u64 v[230:231], s[38:39], 0, v[204:205]
	s_waitcnt lgkmcnt(0)
	ds_read_b128 v[166:169], v245 offset:32768
	ds_read_b128 v[170:173], v245 offset:33792
	ds_read_b128 v[174:177], v245 offset:34816
	ds_read_b128 v[178:181], v245 offset:35840
	ds_read_b128 v[182:185], v245 offset:36864
	ds_read_b128 v[186:189], v245 offset:37888
	ds_read_b128 v[190:193], v245 offset:38912
	ds_read_b128 v[194:197], v245 offset:39936
	global_load_lds_dwordx4 v[230:231], off
	v_lshl_add_u64 v[230:231], s[38:39], 0, v[208:209]
	s_mov_b32 m0, s45
	s_nop 0
	global_load_lds_dwordx4 v[230:231], off
	s_waitcnt vmcnt(8)
	s_waitcnt lgkmcnt(0)
	s_barrier
	s_setprio 1
	s_waitcnt lgkmcnt(0)
	v_mfma_f32_16x16x32_bf16 v[130:133], v[150:153], v[166:169], v[130:133]
	v_mfma_f32_16x16x32_bf16 v[126:129], v[158:161], v[166:169], v[126:129]
	v_mfma_f32_16x16x32_bf16 v[122:125], v[150:153], v[174:177], v[122:125]
	v_mfma_f32_16x16x32_bf16 v[118:121], v[158:161], v[174:177], v[118:121]
	v_mfma_f32_16x16x32_bf16 v[114:117], v[150:153], v[182:185], v[114:117]
	v_mfma_f32_16x16x32_bf16 v[110:113], v[158:161], v[182:185], v[110:113]
	v_mfma_f32_16x16x32_bf16 v[106:109], v[150:153], v[190:193], v[106:109]
	v_mfma_f32_16x16x32_bf16 v[102:105], v[158:161], v[190:193], v[102:105]
	v_mfma_f32_16x16x32_bf16 v[130:133], v[154:157], v[170:173], v[130:133]
	v_mfma_f32_16x16x32_bf16 v[126:129], v[162:165], v[170:173], v[126:129]
	v_mfma_f32_16x16x32_bf16 v[122:125], v[154:157], v[178:181], v[122:125]
	v_mfma_f32_16x16x32_bf16 v[118:121], v[162:165], v[178:181], v[118:121]
	v_mfma_f32_16x16x32_bf16 v[114:117], v[154:157], v[186:189], v[114:117]
	v_mfma_f32_16x16x32_bf16 v[110:113], v[162:165], v[186:189], v[110:113]
	v_mfma_f32_16x16x32_bf16 v[106:109], v[154:157], v[194:197], v[106:109]
	v_mfma_f32_16x16x32_bf16 v[102:105], v[162:165], v[194:197], v[102:105]
	v_mfma_f32_16x16x32_bf16 v[98:101], v[134:137], v[166:169], v[98:101]
	v_mfma_f32_16x16x32_bf16 v[94:97], v[142:145], v[166:169], v[94:97]
	v_mfma_f32_16x16x32_bf16 v[90:93], v[134:137], v[174:177], v[90:93]
	v_mfma_f32_16x16x32_bf16 v[86:89], v[142:145], v[174:177], v[86:89]
	v_mfma_f32_16x16x32_bf16 v[82:85], v[134:137], v[182:185], v[82:85]
	v_mfma_f32_16x16x32_bf16 v[78:81], v[142:145], v[182:185], v[78:81]
	v_mfma_f32_16x16x32_bf16 v[74:77], v[134:137], v[190:193], v[74:77]
	v_mfma_f32_16x16x32_bf16 v[70:73], v[142:145], v[190:193], v[70:73]
	v_mfma_f32_16x16x32_bf16 v[98:101], v[138:141], v[170:173], v[98:101]
	v_mfma_f32_16x16x32_bf16 v[94:97], v[146:149], v[170:173], v[94:97]
	v_mfma_f32_16x16x32_bf16 v[90:93], v[138:141], v[178:181], v[90:93]
	v_mfma_f32_16x16x32_bf16 v[86:89], v[146:149], v[178:181], v[86:89]
	v_mfma_f32_16x16x32_bf16 v[82:85], v[138:141], v[186:189], v[82:85]
	v_mfma_f32_16x16x32_bf16 v[78:81], v[146:149], v[186:189], v[78:81]
	v_mfma_f32_16x16x32_bf16 v[74:77], v[138:141], v[194:197], v[74:77]
	v_mfma_f32_16x16x32_bf16 v[70:73], v[146:149], v[194:197], v[70:73]
	s_setprio 0
	s_barrier
	s_add_i32 s33, s33, s11
	v_lshl_add_u64 v[218:219], v[218:219], 0, s[88:89]
	s_mov_b32 m0, s33
	ds_read_b128 v[190:193], v245 offset:49152
	ds_read_b128 v[194:197], v245 offset:50176
	ds_read_b128 v[182:185], v245 offset:51200
	ds_read_b128 v[186:189], v245 offset:52224
	ds_read_b128 v[174:177], v245 offset:53248
	ds_read_b128 v[178:181], v245 offset:54272
	ds_read_b128 v[166:169], v245 offset:55296
	ds_read_b128 v[170:173], v245 offset:56320
	global_load_lds_dwordx4 v[218:219], off
	s_add_i32 m0, s33, 0x2000
	s_add_u32 s36, s36, 0x20080
	v_lshl_add_u64 v[218:219], v[220:221], 0, s[88:89]
	s_addc_u32 s37, s37, 0
	s_add_i32 s33, s58, s11
	global_load_lds_dwordx4 v[218:219], off
	v_lshl_add_u64 v[218:219], s[36:37], 0, v[206:207]
	s_mov_b32 m0, s33
	s_and_b64 vcc, exec, s[8:9]
	global_load_lds_dwordx4 v[218:219], off
	v_lshl_add_u64 v[218:219], s[36:37], 0, v[210:211]
	s_add_i32 m0, s33, 0x2000
	s_nop 0
	global_load_lds_dwordx4 v[218:219], off
	v_lshl_add_u64 v[218:219], v[222:223], 0, s[88:89]
	s_mov_b32 m0, s46
	s_nop 0
	global_load_lds_dwordx4 v[218:219], off
	v_lshl_add_u64 v[218:219], v[224:225], 0, s[88:89]
	s_mov_b32 m0, s47
	s_nop 0
	global_load_lds_dwordx4 v[218:219], off
	s_waitcnt vmcnt(8)
	s_waitcnt lgkmcnt(0)
	s_barrier
	s_cbranch_vccnz .LBB0_1293
	s_setprio 1
	s_waitcnt lgkmcnt(0)
	v_mfma_f32_16x16x32_bf16 v[66:69], v[150:153], v[190:193], v[66:69]
	v_mfma_f32_16x16x32_bf16 v[62:65], v[158:161], v[190:193], v[62:65]
	v_mfma_f32_16x16x32_bf16 v[58:61], v[150:153], v[182:185], v[58:61]
	v_mfma_f32_16x16x32_bf16 v[54:57], v[158:161], v[182:185], v[54:57]
	v_mfma_f32_16x16x32_bf16 v[50:53], v[150:153], v[174:177], v[50:53]
	v_mfma_f32_16x16x32_bf16 v[46:49], v[158:161], v[174:177], v[46:49]
	v_mfma_f32_16x16x32_bf16 v[42:45], v[150:153], v[166:169], v[42:45]
	v_mfma_f32_16x16x32_bf16 v[38:41], v[158:161], v[166:169], v[38:41]
	v_mfma_f32_16x16x32_bf16 v[66:69], v[154:157], v[194:197], v[66:69]
	v_mfma_f32_16x16x32_bf16 v[62:65], v[162:165], v[194:197], v[62:65]
	v_mfma_f32_16x16x32_bf16 v[58:61], v[154:157], v[186:189], v[58:61]
	v_mfma_f32_16x16x32_bf16 v[54:57], v[162:165], v[186:189], v[54:57]
	v_mfma_f32_16x16x32_bf16 v[50:53], v[154:157], v[178:181], v[50:53]
	v_mfma_f32_16x16x32_bf16 v[46:49], v[162:165], v[178:181], v[46:49]
	v_mfma_f32_16x16x32_bf16 v[42:45], v[154:157], v[170:173], v[42:45]
	v_mfma_f32_16x16x32_bf16 v[38:41], v[162:165], v[170:173], v[38:41]
	v_mfma_f32_16x16x32_bf16 v[30:33], v[134:137], v[190:193], v[30:33]
	v_mfma_f32_16x16x32_bf16 v[26:29], v[142:145], v[190:193], v[26:29]
	v_mfma_f32_16x16x32_bf16 v[22:25], v[134:137], v[182:185], v[22:25]
	v_mfma_f32_16x16x32_bf16 v[18:21], v[142:145], v[182:185], v[18:21]
	v_mfma_f32_16x16x32_bf16 v[14:17], v[134:137], v[174:177], v[14:17]
	v_mfma_f32_16x16x32_bf16 v[10:13], v[142:145], v[174:177], v[10:13]
	v_mfma_f32_16x16x32_bf16 v[6:9], v[134:137], v[166:169], v[6:9]
	v_mfma_f32_16x16x32_bf16 v[2:5], v[142:145], v[166:169], v[2:5]
	v_mfma_f32_16x16x32_bf16 v[30:33], v[138:141], v[194:197], v[30:33]
	v_mfma_f32_16x16x32_bf16 v[26:29], v[146:149], v[194:197], v[26:29]
	v_mfma_f32_16x16x32_bf16 v[22:25], v[138:141], v[186:189], v[22:25]
	v_mfma_f32_16x16x32_bf16 v[18:21], v[146:149], v[186:189], v[18:21]
	v_mfma_f32_16x16x32_bf16 v[14:17], v[138:141], v[178:181], v[14:17]
	v_mfma_f32_16x16x32_bf16 v[10:13], v[146:149], v[178:181], v[10:13]
	v_mfma_f32_16x16x32_bf16 v[6:9], v[138:141], v[170:173], v[6:9]
	v_mfma_f32_16x16x32_bf16 v[2:5], v[146:149], v[170:173], v[2:5]
	s_setprio 0
	s_branch .LBB0_1293
